# attention: QK/PV VALU evenly interleaved with MFMAs, running max folded into accumulator init (20 MFMA/tile); ssd_scan, gemm_out residual epilogue and router row-norm loads pipelined with counted vmcn
# speedup vs baseline: 1.1062x; 1.0729x over previous
.LBB0_847:
	s_mov_b32 s6, 0x2aaaaaab
	v_mul_hi_i32 v2, v14, s6
	v_lshrrev_b32_e32 v3, 31, v2
	v_ashrrev_i32_e32 v2, 13, v2
	v_add_u32_e32 v3, v2, v3
	v_mul_i32_i24_e32 v2, 0xc000, v3
	v_sub_u32_e32 v6, v14, v2
	v_lshrrev_b32_e32 v7, 13, v6
	v_mul_u32_u24_e32 v4, 0x82, v3
	s_mov_b32 s6, 0xc000
	v_mul_lo_u32 v5, v4, s6
	v_add_u32_e32 v5, v5, v6
	v_lshlrev_b32_e32 v8, 2, v5
	v_lshlrev_b32_e32 v9, 1, v5
	v_lshlrev_b32_e32 v4, 3, v4
	v_add_u32_e32 v4, v4, v7
	v_lshlrev_b32_e32 v10, 2, v4
	s_add_u32 s4, s2, 0x35fb0000
	s_addc_u32 s5, s3, 0
	s_add_u32 s6, s2, 0x70e34100
	s_addc_u32 s7, s3, 0
	s_add_u32 s8, s2, 0x3c130000
	s_addc_u32 s9, s3, 0
	v_mov_b32_e32 v15, 0
	s_movk_i32 s25, 0x7fff
	global_load_dword v20, v8, s[4:5]
	s_add_u32 s4, s4, 0x30000
	s_addc_u32 s5, s5, 0
	global_load_dword v21, v8, s[4:5]
	s_add_u32 s4, s4, 0x30000
	s_addc_u32 s5, s5, 0
	global_load_dword v22, v8, s[4:5]
	s_add_u32 s4, s4, 0x30000
	s_addc_u32 s5, s5, 0
	global_load_dword v23, v8, s[4:5]
	s_add_u32 s4, s4, 0x30000
	s_addc_u32 s5, s5, 0
	global_load_dword v24, v8, s[4:5]
	s_add_u32 s4, s4, 0x30000
	s_addc_u32 s5, s5, 0
	global_load_dword v25, v8, s[4:5]
	s_add_u32 s4, s4, 0x30000
	s_addc_u32 s5, s5, 0
	global_load_dword v26, v8, s[4:5]
	s_add_u32 s4, s4, 0x30000
	s_addc_u32 s5, s5, 0
	global_load_dword v27, v8, s[4:5]
	s_add_u32 s4, s4, 0x30000
	s_addc_u32 s5, s5, 0
	global_load_dword v28, v8, s[4:5]
	s_add_u32 s4, s4, 0x30000
	s_addc_u32 s5, s5, 0
	global_load_dword v29, v8, s[4:5]
	s_add_u32 s4, s4, 0x30000
	s_addc_u32 s5, s5, 0
	global_load_dword v30, v10, s[8:9] offset:0
	global_load_dword v31, v10, s[8:9] offset:32
	global_load_dword v32, v10, s[8:9] offset:64
	global_load_dword v33, v10, s[8:9] offset:96
	global_load_dword v34, v10, s[8:9] offset:128
	global_load_dword v35, v10, s[8:9] offset:160
	global_load_dword v36, v10, s[8:9] offset:192
	global_load_dword v37, v10, s[8:9] offset:224
	global_load_dword v38, v10, s[8:9] offset:256
	global_load_dword v39, v10, s[8:9] offset:288
	s_add_u32 s8, s8, 0x140
	s_addc_u32 s9, s9, 0
	s_mov_b32 s24, 0
.Lscan_loop:
	global_load_dword v40, v8, s[4:5]
	s_add_u32 s4, s4, 0x30000
	s_addc_u32 s5, s5, 0
	global_load_dword v41, v8, s[4:5]
	s_add_u32 s4, s4, 0x30000
	s_addc_u32 s5, s5, 0
	global_load_dword v42, v8, s[4:5]
	s_add_u32 s4, s4, 0x30000
	s_addc_u32 s5, s5, 0
	global_load_dword v43, v8, s[4:5]
	s_add_u32 s4, s4, 0x30000
	s_addc_u32 s5, s5, 0
	global_load_dword v44, v8, s[4:5]
	s_add_u32 s4, s4, 0x30000
	s_addc_u32 s5, s5, 0
	global_load_dword v45, v8, s[4:5]
	s_add_u32 s4, s4, 0x30000
	s_addc_u32 s5, s5, 0
	global_load_dword v46, v8, s[4:5]
	s_add_u32 s4, s4, 0x30000
	s_addc_u32 s5, s5, 0
	global_load_dword v47, v8, s[4:5]
	s_add_u32 s4, s4, 0x30000
	s_addc_u32 s5, s5, 0
	global_load_dword v48, v8, s[4:5]
	s_add_u32 s4, s4, 0x30000
	s_addc_u32 s5, s5, 0
	global_load_dword v49, v8, s[4:5]
	s_add_u32 s4, s4, 0x30000
	s_addc_u32 s5, s5, 0
	global_load_dword v51, v10, s[8:9] offset:0
	global_load_dword v52, v10, s[8:9] offset:32
	global_load_dword v53, v10, s[8:9] offset:64
	global_load_dword v54, v10, s[8:9] offset:96
	global_load_dword v55, v10, s[8:9] offset:128
	global_load_dword v56, v10, s[8:9] offset:160
	global_load_dword v57, v10, s[8:9] offset:192
	global_load_dword v58, v10, s[8:9] offset:224
	global_load_dword v59, v10, s[8:9] offset:256
	global_load_dword v60, v10, s[8:9] offset:288
	s_add_u32 s8, s8, 0x140
	s_addc_u32 s9, s9, 0
	s_waitcnt vmcnt(20)
	v_bfe_u32 v16, v15, 16, 1
	v_add3_u32 v16, v15, v16, s25
	global_store_short_d16_hi v9, v16, s[6:7]
	s_add_u32 s6, s6, 0x18000
	s_addc_u32 s7, s7, 0
	v_fma_f32 v15, v15, v30, v20
	v_bfe_u32 v16, v15, 16, 1
	v_add3_u32 v16, v15, v16, s25
	global_store_short_d16_hi v9, v16, s[6:7]
	s_add_u32 s6, s6, 0x18000
	s_addc_u32 s7, s7, 0
	v_fma_f32 v15, v15, v31, v21
	v_bfe_u32 v16, v15, 16, 1
	v_add3_u32 v16, v15, v16, s25
	global_store_short_d16_hi v9, v16, s[6:7]
	s_add_u32 s6, s6, 0x18000
	s_addc_u32 s7, s7, 0
	v_fma_f32 v15, v15, v32, v22
	v_bfe_u32 v16, v15, 16, 1
	v_add3_u32 v16, v15, v16, s25
	global_store_short_d16_hi v9, v16, s[6:7]
	s_add_u32 s6, s6, 0x18000
	s_addc_u32 s7, s7, 0
	v_fma_f32 v15, v15, v33, v23
	v_bfe_u32 v16, v15, 16, 1
	v_add3_u32 v16, v15, v16, s25
	global_store_short_d16_hi v9, v16, s[6:7]
	s_add_u32 s6, s6, 0x18000
	s_addc_u32 s7, s7, 0
	v_fma_f32 v15, v15, v34, v24
	v_bfe_u32 v16, v15, 16, 1
	v_add3_u32 v16, v15, v16, s25
	global_store_short_d16_hi v9, v16, s[6:7]
	s_add_u32 s6, s6, 0x18000
	s_addc_u32 s7, s7, 0
	v_fma_f32 v15, v15, v35, v25
	v_bfe_u32 v16, v15, 16, 1
	v_add3_u32 v16, v15, v16, s25
	global_store_short_d16_hi v9, v16, s[6:7]
	s_add_u32 s6, s6, 0x18000
	s_addc_u32 s7, s7, 0
	v_fma_f32 v15, v15, v36, v26
	v_bfe_u32 v16, v15, 16, 1
	v_add3_u32 v16, v15, v16, s25
	global_store_short_d16_hi v9, v16, s[6:7]
	s_add_u32 s6, s6, 0x18000
	s_addc_u32 s7, s7, 0
	v_fma_f32 v15, v15, v37, v27
	v_bfe_u32 v16, v15, 16, 1
	v_add3_u32 v16, v15, v16, s25
	global_store_short_d16_hi v9, v16, s[6:7]
	s_add_u32 s6, s6, 0x18000
	s_addc_u32 s7, s7, 0
	v_fma_f32 v15, v15, v38, v28
	v_bfe_u32 v16, v15, 16, 1
	v_add3_u32 v16, v15, v16, s25
	global_store_short_d16_hi v9, v16, s[6:7]
	s_add_u32 s6, s6, 0x18000
	s_addc_u32 s7, s7, 0
	v_fma_f32 v15, v15, v39, v29
	global_load_dword v20, v8, s[4:5]
	s_add_u32 s4, s4, 0x30000
	s_addc_u32 s5, s5, 0
	global_load_dword v21, v8, s[4:5]
	s_add_u32 s4, s4, 0x30000
	s_addc_u32 s5, s5, 0
	global_load_dword v22, v8, s[4:5]
	s_add_u32 s4, s4, 0x30000
	s_addc_u32 s5, s5, 0
	global_load_dword v23, v8, s[4:5]
	s_add_u32 s4, s4, 0x30000
	s_addc_u32 s5, s5, 0
	global_load_dword v24, v8, s[4:5]
	s_add_u32 s4, s4, 0x30000
	s_addc_u32 s5, s5, 0
	global_load_dword v25, v8, s[4:5]
	s_add_u32 s4, s4, 0x30000
	s_addc_u32 s5, s5, 0
	global_load_dword v26, v8, s[4:5]
	s_add_u32 s4, s4, 0x30000
	s_addc_u32 s5, s5, 0
	global_load_dword v27, v8, s[4:5]
	s_add_u32 s4, s4, 0x30000
	s_addc_u32 s5, s5, 0
	global_load_dword v28, v8, s[4:5]
	s_add_u32 s4, s4, 0x30000
	s_addc_u32 s5, s5, 0
	global_load_dword v29, v8, s[4:5]
	s_add_u32 s4, s4, 0x30000
	s_addc_u32 s5, s5, 0
	global_load_dword v30, v10, s[8:9] offset:0
	global_load_dword v31, v10, s[8:9] offset:32
	global_load_dword v32, v10, s[8:9] offset:64
	global_load_dword v33, v10, s[8:9] offset:96
	global_load_dword v34, v10, s[8:9] offset:128
	global_load_dword v35, v10, s[8:9] offset:160
	global_load_dword v36, v10, s[8:9] offset:192
	global_load_dword v37, v10, s[8:9] offset:224
	global_load_dword v38, v10, s[8:9] offset:256
	global_load_dword v39, v10, s[8:9] offset:288
	s_add_u32 s8, s8, 0x140
	s_addc_u32 s9, s9, 0
	s_waitcnt vmcnt(20)
	v_bfe_u32 v16, v15, 16, 1
	v_add3_u32 v16, v15, v16, s25
	global_store_short_d16_hi v9, v16, s[6:7]
	s_add_u32 s6, s6, 0x18000
	s_addc_u32 s7, s7, 0
	v_fma_f32 v15, v15, v51, v40
	v_bfe_u32 v16, v15, 16, 1
	v_add3_u32 v16, v15, v16, s25
	global_store_short_d16_hi v9, v16, s[6:7]
	s_add_u32 s6, s6, 0x18000
	s_addc_u32 s7, s7, 0
	v_fma_f32 v15, v15, v52, v41
	v_bfe_u32 v16, v15, 16, 1
	v_add3_u32 v16, v15, v16, s25
	global_store_short_d16_hi v9, v16, s[6:7]
	s_add_u32 s6, s6, 0x18000
	s_addc_u32 s7, s7, 0
	v_fma_f32 v15, v15, v53, v42
	v_bfe_u32 v16, v15, 16, 1
	v_add3_u32 v16, v15, v16, s25
	global_store_short_d16_hi v9, v16, s[6:7]
	s_add_u32 s6, s6, 0x18000
	s_addc_u32 s7, s7, 0
	v_fma_f32 v15, v15, v54, v43
	v_bfe_u32 v16, v15, 16, 1
	v_add3_u32 v16, v15, v16, s25
	global_store_short_d16_hi v9, v16, s[6:7]
	s_add_u32 s6, s6, 0x18000
	s_addc_u32 s7, s7, 0
	v_fma_f32 v15, v15, v55, v44
	v_bfe_u32 v16, v15, 16, 1
	v_add3_u32 v16, v15, v16, s25
	global_store_short_d16_hi v9, v16, s[6:7]
	s_add_u32 s6, s6, 0x18000
	s_addc_u32 s7, s7, 0
	v_fma_f32 v15, v15, v56, v45
	v_bfe_u32 v16, v15, 16, 1
	v_add3_u32 v16, v15, v16, s25
	global_store_short_d16_hi v9, v16, s[6:7]
	s_add_u32 s6, s6, 0x18000
	s_addc_u32 s7, s7, 0
	v_fma_f32 v15, v15, v57, v46
	v_bfe_u32 v16, v15, 16, 1
	v_add3_u32 v16, v15, v16, s25
	global_store_short_d16_hi v9, v16, s[6:7]
	s_add_u32 s6, s6, 0x18000
	s_addc_u32 s7, s7, 0
	v_fma_f32 v15, v15, v58, v47
	v_bfe_u32 v16, v15, 16, 1
	v_add3_u32 v16, v15, v16, s25
	global_store_short_d16_hi v9, v16, s[6:7]
	s_add_u32 s6, s6, 0x18000
	s_addc_u32 s7, s7, 0
	v_fma_f32 v15, v15, v59, v48
	v_bfe_u32 v16, v15, 16, 1
	v_add3_u32 v16, v15, v16, s25
	global_store_short_d16_hi v9, v16, s[6:7]
	s_add_u32 s6, s6, 0x18000
	s_addc_u32 s7, s7, 0
	v_fma_f32 v15, v15, v60, v49
	s_add_i32 s24, s24, 1
	s_cmp_lt_u32 s24, 6
	s_cbranch_scc1 .Lscan_loop
	s_waitcnt vmcnt(0)
	v_bfe_u32 v16, v15, 16, 1
	v_add3_u32 v16, v15, v16, s25
	global_store_short_d16_hi v9, v16, s[6:7]
	s_add_u32 s6, s6, 0x18000
	s_addc_u32 s7, s7, 0
	v_fma_f32 v15, v15, v30, v20
	v_bfe_u32 v16, v15, 16, 1
	v_add3_u32 v16, v15, v16, s25
	global_store_short_d16_hi v9, v16, s[6:7]
	s_add_u32 s6, s6, 0x18000
	s_addc_u32 s7, s7, 0
	v_fma_f32 v15, v15, v31, v21
	v_bfe_u32 v16, v15, 16, 1
	v_add3_u32 v16, v15, v16, s25
	global_store_short_d16_hi v9, v16, s[6:7]
	s_add_u32 s6, s6, 0x18000
	s_addc_u32 s7, s7, 0
	v_fma_f32 v15, v15, v32, v22
	v_bfe_u32 v16, v15, 16, 1
	v_add3_u32 v16, v15, v16, s25
	global_store_short_d16_hi v9, v16, s[6:7]
	s_add_u32 s6, s6, 0x18000
	s_addc_u32 s7, s7, 0
	v_fma_f32 v15, v15, v33, v23
	v_bfe_u32 v16, v15, 16, 1
	v_add3_u32 v16, v15, v16, s25
	global_store_short_d16_hi v9, v16, s[6:7]
	s_add_u32 s6, s6, 0x18000
	s_addc_u32 s7, s7, 0
	v_fma_f32 v15, v15, v34, v24
	v_bfe_u32 v16, v15, 16, 1
	v_add3_u32 v16, v15, v16, s25
	global_store_short_d16_hi v9, v16, s[6:7]
	s_add_u32 s6, s6, 0x18000
	s_addc_u32 s7, s7, 0
	v_fma_f32 v15, v15, v35, v25
	v_bfe_u32 v16, v15, 16, 1
	v_add3_u32 v16, v15, v16, s25
	global_store_short_d16_hi v9, v16, s[6:7]
	s_add_u32 s6, s6, 0x18000
	s_addc_u32 s7, s7, 0
	v_fma_f32 v15, v15, v36, v26
	v_bfe_u32 v16, v15, 16, 1
	v_add3_u32 v16, v15, v16, s25
	global_store_short_d16_hi v9, v16, s[6:7]
	s_add_u32 s6, s6, 0x18000
	s_addc_u32 s7, s7, 0
	v_fma_f32 v15, v15, v37, v27
	v_bfe_u32 v16, v15, 16, 1
	v_add3_u32 v16, v15, v16, s25
	global_store_short_d16_hi v9, v16, s[6:7]
	s_add_u32 s6, s6, 0x18000
	s_addc_u32 s7, s7, 0
	v_fma_f32 v15, v15, v38, v28
	v_bfe_u32 v16, v15, 16, 1
	v_add3_u32 v16, v15, v16, s25
	global_store_short_d16_hi v9, v16, s[6:7]
	s_add_u32 s6, s6, 0x18000
	s_addc_u32 s7, s7, 0
	v_fma_f32 v15, v15, v39, v29

.LBB0_1428:
	s_or_b64 exec, exec, s[10:11]
	v_and_b32_e32 v140, 0xffffffe0, v39
	s_movk_i32 s20, 0xc0
	v_mov_b32_e32 v39, v83
	v_add_u32_e32 v44, 64, v40
	v_mov_b64_e32 v[42:43], s[8:9]
	v_lshl_add_u64 v[38:39], s[8:9], 0, v[38:39]
	v_sub_f32_e32 v46, v18, v159
	v_add_co_u32_e32 v18, vcc, s66, v34
	v_mad_i64_i32 v[44:45], s[8:9], v44, s20, v[42:43]
	v_sub_f32_e32 v47, v19, v159
	v_addc_co_u32_e32 v19, vcc, 0, v35, vcc
	v_lshlrev_b64 v[70:71], 1, v[36:37]
	s_movk_i32 s8, 0x3000
	v_lshl_add_u64 v[36:37], v[44:45], 0, v[70:71]
	global_load_dwordx4 v[56:59], v[18:19], off
	global_load_dwordx4 v[60:63], v[36:37], off
	v_add_co_u32_e32 v18, vcc, s8, v38
	s_movk_i32 s8, 0x6000
	s_nop 0
	v_addc_co_u32_e32 v19, vcc, 0, v39, vcc
	global_load_dwordx4 v[64:67], v[18:19], off
	v_sub_f32_e32 v18, v20, v159
	v_sub_f32_e32 v19, v21, v159
	v_exp_f32_e32 v227, v18
	v_add_co_u32_e32 v18, vcc, s8, v38
	v_exp_f32_e32 v230, v19
	s_nop 0
	v_addc_co_u32_e32 v19, vcc, 0, v39, vcc
	global_load_dwordx4 v[122:125], v[18:19], off
	v_add_u32_e32 v18, 0x80, v40
	v_sub_f32_e32 v20, v22, v159
	v_mad_i64_i32 v[18:19], s[8:9], v18, s20, v[42:43]
	v_sub_f32_e32 v21, v23, v159
	v_exp_f32_e32 v231, v20
	v_lshl_add_u64 v[18:19], v[18:19], 0, v[70:71]
	v_add_co_u32_e32 v20, vcc, s69, v34
	v_exp_f32_e32 v232, v21
	s_nop 0
	v_addc_co_u32_e32 v21, vcc, 0, v35, vcc
	global_load_dwordx4 v[118:121], v[18:19], off
	global_load_dwordx4 v[114:117], v[20:21], off
	v_mad_i64_i32 v[68:69], s[10:11], v40, s20, 0
	s_movk_i32 s11, 0x200
	v_sub_f32_e32 v34, v2, v159
	v_or_b32_sdwa v2, v52, s11 dst_sel:DWORD dst_unused:UNUSED_PAD src0_sel:BYTE_0 src1_sel:DWORD
	s_mov_b32 s11, 0x15555556
	v_sub_f32_e32 v36, v4, v159
	v_sub_f32_e32 v35, v3, v159
	v_mul_hi_u32 v4, v2, s11
	v_mov_b64_e32 v[2:3], s[4:5]
	s_mov_b32 s11, 0xffff
	v_and_b32_e32 v18, 0x3fffffc0, v52
	v_readlane_b32 s8, v252, 28
	v_lshlrev_b32_e32 v19, 4, v41
	v_mad_u64_u32 v[2:3], s[20:21], v4, s20, v[2:3]
	v_and_b32_sdwa v4, s11, v53 dst_sel:DWORD dst_unused:UNUSED_PAD src0_sel:DWORD src1_sel:WORD_1
	v_sub_f32_e32 v22, v24, v159
	v_sub_f32_e32 v23, v25, v159
	v_sub_f32_e32 v24, v26, v159
	v_sub_f32_e32 v25, v27, v159
	v_sub_f32_e32 v26, v28, v159
	v_sub_f32_e32 v27, v29, v159
	v_sub_f32_e32 v28, v30, v159
	v_sub_f32_e32 v29, v31, v159
	v_sub_f32_e32 v30, v32, v159
	v_sub_f32_e32 v31, v33, v159
	v_lshl_add_u32 v141, v18, 2, s8
	v_lshlrev_b32_e32 v18, 3, v41
	v_and_b32_e32 v19, 0xc0, v19
	v_lshlrev_b32_e32 v20, 1, v41
	v_sub_f32_e32 v37, v5, v159
	v_lshlrev_b32_e32 v4, 1, v4
	v_mov_b32_e32 v5, v83
	v_exp_f32_e32 v222, v46
	v_exp_f32_e32 v223, v47
	v_exp_f32_e32 v233, v22
	v_exp_f32_e32 v234, v23
	v_exp_f32_e32 v235, v24
	v_exp_f32_e32 v236, v25
	v_exp_f32_e32 v237, v26
	v_exp_f32_e32 v238, v27
	v_exp_f32_e32 v239, v28
	v_exp_f32_e32 v240, v29
	v_exp_f32_e32 v241, v30
	v_exp_f32_e32 v246, v31
	v_and_or_b32 v19, v18, 24, v19
	v_and_b32_e32 v20, 32, v20
	v_and_b32_e32 v18, 0x100, v18
	v_lshl_add_u64 v[142:143], v[2:3], 0, v[4:5]
	v_lshl_add_u64 v[2:3], s[4:5], 0, v[68:69]
	v_and_b32_e32 v4, 7, v52
	v_or3_b32 v18, v19, v20, v18
	v_sub_f32_e32 v49, v17, v159
	v_sub_f32_e32 v48, v16, v159
	s_waitcnt vmcnt(3)
	v_lshl_add_u64 v[144:145], v[2:3], 0, v[70:71]
	v_lshl_add_u64 v[2:3], s[6:7], 0, v[50:51]
	v_lshlrev_b32_e32 v4, 4, v4
	v_mov_b32_e32 v16, v83
	v_mov_b32_e32 v17, v83
	v_add_u32_e32 v158, 0, v18
	v_sub_f32_e32 v47, v15, v159
	v_sub_f32_e32 v46, v14, v159
	v_sub_f32_e32 v45, v13, v159
	v_sub_f32_e32 v44, v12, v159
	v_sub_f32_e32 v43, v11, v159
	v_sub_f32_e32 v42, v10, v159
	v_sub_f32_e32 v41, v9, v159
	v_sub_f32_e32 v40, v8, v159
	v_sub_f32_e32 v39, v7, v159
	v_sub_f32_e32 v38, v6, v159
	v_lshl_add_u64 v[146:147], v[2:3], 0, v[4:5]
	v_mov_b32_e32 v2, v83
	v_mov_b32_e32 v3, v83
	v_mov_b32_e32 v4, v83
	v_mov_b32_e32 v6, v83
	v_mov_b32_e32 v7, v83
	v_mov_b32_e32 v8, v83
	v_mov_b32_e32 v9, v83
	v_mov_b32_e32 v10, v83
	v_mov_b32_e32 v11, v83
	v_mov_b32_e32 v12, v83
	v_mov_b32_e32 v13, v83
	v_mov_b32_e32 v14, v83
	v_mov_b32_e32 v15, v83
	v_mov_b64_e32 v[32:33], v[16:17]
	s_ashr_i32 s3, s2, 31
	s_mov_b32 s22, 2
	s_mov_b32 s8, 4
	s_mov_b32 s10, 1
	s_mov_b32 s9, 0
	v_lshl_add_u32 v156, v139, 2, v141
	v_mov_b32_e32 v157, 0
	v_mov_b32_e32 v169, 1.0
	v_mov_b64_e32 v[30:31], v[14:15]
	v_mov_b64_e32 v[28:29], v[12:13]
	v_mov_b64_e32 v[26:27], v[10:11]
	v_mov_b64_e32 v[24:25], v[8:9]
	v_mov_b64_e32 v[22:23], v[6:7]
	v_mov_b64_e32 v[20:21], v[4:5]
	v_mov_b64_e32 v[18:19], v[2:3]
	s_waitcnt vmcnt(5)
	ds_write_b128 v165, v[56:59] offset:8192
	s_waitcnt vmcnt(4)
	ds_write_b128 v54, v[60:63] offset:40960
	s_waitcnt vmcnt(3)
	ds_write_b128 v55, v[64:67] offset:40960
	s_waitcnt lgkmcnt(0)
	s_barrier
	v_subrev_u32_e32 v142, s4, v142
	v_subrev_u32_e32 v144, s4, v144
	v_subrev_u32_e32 v146, s6, v146
	s_add_u32 s82, s14, s4
	s_addc_u32 s83, s15, s5
	s_add_u32 s82, s82, 0x9000
	s_addc_u32 s83, s83, 0
	s_add_u32 s84, s16, s6
	s_addc_u32 s85, s17, s7
	s_add_u32 s84, s84, 0x6000
	s_addc_u32 s85, s85, 0
	v_xor_b32_e32 v188, 0x80000000, v159
	v_xor_b32_e32 v189, 0x80000000, v159
	v_xor_b32_e32 v190, 0x80000000, v159
	v_xor_b32_e32 v191, 0x80000000, v159
	v_xor_b32_e32 v192, 0x80000000, v159
	v_xor_b32_e32 v193, 0x80000000, v159
	v_xor_b32_e32 v194, 0x80000000, v159
	v_xor_b32_e32 v195, 0x80000000, v159
	v_xor_b32_e32 v196, 0x80000000, v159
	v_xor_b32_e32 v197, 0x80000000, v159
	v_xor_b32_e32 v198, 0x80000000, v159
	v_xor_b32_e32 v199, 0x80000000, v159
	v_xor_b32_e32 v200, 0x80000000, v159
	v_xor_b32_e32 v201, 0x80000000, v159
	v_xor_b32_e32 v202, 0x80000000, v159
	v_xor_b32_e32 v203, 0x80000000, v159
.LBB0_1429:
	s_mov_b32 s4, s9
	s_mov_b32 s9, s22
	s_lshl_b32 s5, s10, 14
	s_add_i32 s5, s5, 0
	v_add_u32_e32 v54, s5, v167
	ds_read_b128 v[50:53], v54 offset:24576
	ds_read_b128 v[54:57], v54 offset:32768
	v_add_u32_e32 v148, s5, v168
	ds_read_b128 v[170:173], v148 offset:24576
	ds_read_b128 v[174:177], v148 offset:32768
	v_add_u32_e32 v148, s5, v166
	s_waitcnt lgkmcnt(3)
	v_mfma_f32_32x32x16_bf16 v[66:81], v[50:53], v[106:109], v[188:203]
	v_exp_f32_e32 v178, v42
	v_exp_f32_e32 v179, v43
	v_exp_f32_e32 v180, v44
	v_add_f32_e32 v143, v222, v227
	s_waitcnt lgkmcnt(2)
	v_mfma_f32_32x32x16_bf16 v[50:65], v[54:57], v[106:109], v[188:203]
	v_exp_f32_e32 v181, v45
	v_exp_f32_e32 v182, v46
	v_exp_f32_e32 v183, v47
	v_add_f32_e32 v145, v223, v230
	s_waitcnt lgkmcnt(1)
	v_mfma_f32_32x32x16_bf16 v[66:81], v[170:173], v[102:105], v[66:81]
	v_exp_f32_e32 v184, v48
	v_exp_f32_e32 v49, v49
	v_exp_f32_e32 v153, v35
	v_add_f32_e32 v143, v231, v143
	s_waitcnt lgkmcnt(0)
	v_mfma_f32_32x32x16_bf16 v[50:65], v[174:177], v[102:105], v[50:65]
	v_exp_f32_e32 v185, v34
	v_exp_f32_e32 v186, v36
	v_exp_f32_e32 v187, v37
	v_add_f32_e32 v145, v232, v145
	ds_read_b128 v[170:173], v148 offset:24576
	ds_read_b128 v[174:177], v148 offset:32768
	v_add_u32_e32 v148, s5, v162
	s_waitcnt lgkmcnt(1)
	v_mfma_f32_32x32x16_bf16 v[66:81], v[170:173], v[98:101], v[66:81]
	v_exp_f32_e32 v147, v38
	v_exp_f32_e32 v152, v39
	v_exp_f32_e32 v204, v40
	v_add_f32_e32 v143, v233, v143
	s_waitcnt lgkmcnt(0)
	v_mfma_f32_32x32x16_bf16 v[50:65], v[174:177], v[98:101], v[50:65]
	v_exp_f32_e32 v205, v41
	v_add_f32_e32 v145, v234, v145
	v_add_f32_e32 v143, v235, v143
	v_add_f32_e32 v145, v236, v145
	v_add_f32_e32 v143, v237, v143
	v_add_f32_e32 v145, v238, v145
	ds_read_b128 v[170:173], v148 offset:24576
	ds_read_b128 v[174:177], v148 offset:32768
	v_add_u32_e32 v148, s5, v161
	s_waitcnt lgkmcnt(1)
	v_mfma_f32_32x32x16_bf16 v[66:81], v[170:173], v[94:97], v[66:81]
	v_add_f32_e32 v143, v239, v143
	v_add_f32_e32 v145, v240, v145
	v_add_f32_e32 v143, v241, v143
	v_add_f32_e32 v145, v246, v145
	v_add_f32_e32 v143, v185, v143
	v_add_f32_e32 v145, v153, v145
	v_add_f32_e32 v143, v186, v143
	s_waitcnt lgkmcnt(0)
	v_mfma_f32_32x32x16_bf16 v[50:65], v[174:177], v[94:97], v[50:65]
	v_add_f32_e32 v145, v187, v145
	v_add_f32_e32 v143, v147, v143
	v_add_f32_e32 v145, v152, v145
	v_add_f32_e32 v143, v204, v143
	v_add_f32_e32 v145, v205, v145
	v_add_f32_e32 v143, v178, v143
	v_add_f32_e32 v145, v179, v145
	ds_read_b128 v[170:173], v148 offset:24576
	ds_read_b128 v[174:177], v148 offset:32768
	v_add_u32_e32 v148, s5, v160
	v_lshl_add_u32 v247, s4, 13, v158
	ds_read_b64_tr_b16 v[206:207], v247 offset:0
	ds_read_b64_tr_b16 v[208:209], v247 offset:0x400
	ds_read_b64_tr_b16 v[210:211], v247 offset:0x800
	ds_read_b64_tr_b16 v[212:213], v247 offset:0xc00
	ds_read_b64_tr_b16 v[214:215], v247 offset:0x1000
	ds_read_b64_tr_b16 v[216:217], v247 offset:0x1400
	ds_read_b64_tr_b16 v[218:219], v247 offset:0x1800
	ds_read_b64_tr_b16 v[220:221], v247 offset:0x1c00
	s_waitcnt lgkmcnt(9)
	v_mfma_f32_32x32x16_bf16 v[66:81], v[170:173], v[90:93], v[66:81]
	v_add_f32_e32 v143, v180, v143
	v_add_f32_e32 v145, v181, v145
	v_add_f32_e32 v143, v182, v143
	v_add_f32_e32 v145, v183, v145
	v_add_f32_e32 v143, v184, v143
	v_add_f32_e32 v145, v49, v145
	v_cvt_pk_bf16_f32 v34, v222, v223
	s_waitcnt lgkmcnt(8)
	v_mfma_f32_32x32x16_bf16 v[50:65], v[174:177], v[90:93], v[50:65]
	v_cvt_pk_bf16_f32 v35, v227, v230
	v_cvt_pk_bf16_f32 v36, v231, v232
	v_cvt_pk_bf16_f32 v37, v233, v234
	v_cvt_pk_bf16_f32 v38, v235, v236
	v_cvt_pk_bf16_f32 v39, v237, v238
	v_cvt_pk_bf16_f32 v40, v239, v240
	v_cvt_pk_bf16_f32 v41, v241, v246
	ds_read_b128 v[170:173], v148 offset:24576
	ds_read_b128 v[174:177], v148 offset:32768
	s_waitcnt lgkmcnt(1)
	v_mfma_f32_32x32x16_bf16 v[66:81], v[170:173], v[86:89], v[66:81]
	v_cvt_pk_bf16_f32 v42, v185, v153
	v_cvt_pk_bf16_f32 v43, v186, v187
	v_cvt_pk_bf16_f32 v44, v147, v152
	v_cvt_pk_bf16_f32 v45, v204, v205
	v_cvt_pk_bf16_f32 v46, v178, v179
	v_cvt_pk_bf16_f32 v47, v180, v181
	v_cvt_pk_bf16_f32 v48, v182, v183
	s_waitcnt lgkmcnt(0)
	v_mfma_f32_32x32x16_bf16 v[50:65], v[174:177], v[86:89], v[50:65]
	v_cvt_pk_bf16_f32 v49, v184, v49
	v_add_f32_e32 v170, v143, v145
	global_load_dwordx4 v[130:133], v146, s[84:85]
	global_load_dwordx4 v[126:129], v144, s[82:83]
	global_load_dwordx4 v[134:137], v142, s[82:83]
	s_add_u32 s82, s82, 0x3000
	s_addc_u32 s83, s83, 0
	s_add_u32 s84, s84, 0x2000
	s_addc_u32 s85, s85, 0
	s_waitcnt lgkmcnt(0)
	s_nop 0
	v_mfma_f32_32x32x16_bf16 v[2:17], v[34:37], v[206:209], v[2:17]
	ds_read_b64_tr_b16 v[172:173], v247 offset:0x200
	ds_read_b64_tr_b16 v[174:175], v247 offset:0x600
	v_max_f32_e32 v249, v67, v67
	v_max_f32_e32 v248, v66, v66
	v_max_f32_e32 v248, v248, v249
	v_max3_f32 v248, v248, v68, v69
	v_exp_f32_e32 v222, v66
	v_mfma_f32_32x32x16_bf16 v[2:17], v[38:41], v[210:213], v[2:17]
	ds_read_b64_tr_b16 v[176:177], v247 offset:0xa00
	ds_read_b64_tr_b16 v[178:179], v247 offset:0xe00
	v_max3_f32 v248, v248, v70, v71
	v_max3_f32 v248, v248, v72, v73
	v_max3_f32 v248, v248, v74, v75
	v_exp_f32_e32 v223, v67
	v_exp_f32_e32 v227, v68
	v_mfma_f32_32x32x16_bf16 v[2:17], v[42:45], v[214:217], v[2:17]
	ds_read_b64_tr_b16 v[180:181], v247 offset:0x1200
	ds_read_b64_tr_b16 v[182:183], v247 offset:0x1600
	v_max3_f32 v248, v248, v76, v77
	v_max3_f32 v248, v248, v78, v79
	v_max3_f32 v248, v248, v80, v81
	v_exp_f32_e32 v230, v69
	v_exp_f32_e32 v231, v70
	v_mfma_f32_32x32x16_bf16 v[2:17], v[46:49], v[218:221], v[2:17]
	ds_read_b64_tr_b16 v[184:185], v247 offset:0x1a00
	ds_read_b64_tr_b16 v[186:187], v247 offset:0x1e00
	v_max3_f32 v248, v248, v50, v51
	v_max3_f32 v248, v248, v52, v53
	v_max3_f32 v248, v248, v54, v55
	v_exp_f32_e32 v232, v71
	v_exp_f32_e32 v233, v72
	s_lshl_b32 s11, s9, 13
	s_lshl_b32 s4, s9, 14
	s_add_i32 s6, s4, 0
	s_waitcnt vmcnt(3)
	v_add_u32_e32 v247, s11, v165
	ds_write_b128 v247, v[114:117]
	v_add_u32_e32 v247, s6, v163
	ds_write_b128 v247, v[118:121] offset:24576
	v_add_u32_e32 v247, s6, v164
	ds_write_b128 v247, v[122:125] offset:24576
	s_waitcnt lgkmcnt(3)
	v_mfma_f32_32x32x16_bf16 v[18:33], v[34:37], v[172:175], v[18:33]
	v_max3_f32 v248, v248, v56, v57
	v_max3_f32 v248, v248, v58, v59
	v_max3_f32 v248, v248, v60, v61
	v_exp_f32_e32 v234, v73
	v_exp_f32_e32 v235, v74
	v_mfma_f32_32x32x16_bf16 v[18:33], v[38:41], v[176:179], v[18:33]
	v_max3_f32 v248, v248, v62, v63
	v_max3_f32 v248, v248, v64, v65
	v_exp_f32_e32 v236, v75
	v_exp_f32_e32 v237, v76
	v_exp_f32_e32 v238, v77
	v_mfma_f32_32x32x16_bf16 v[18:33], v[42:45], v[180:183], v[18:33]
	v_exp_f32_e32 v239, v78
	v_exp_f32_e32 v240, v79
	v_exp_f32_e32 v241, v80
	v_exp_f32_e32 v246, v81
	s_mov_b32 s4, 0x41380000
	v_cmp_ge_f32_e32 vcc, s4, v248
	v_mfma_f32_32x32x16_bf16 v[18:33], v[46:49], v[184:187], v[18:33]
	s_cmp_eq_u64 vcc, exec
	s_cbranch_scc0 .LBB0_1448
	v_mov_b32_e32 v172, 1.0
.LBB0_1437:
	s_waitcnt lgkmcnt(0)
	s_barrier
	v_add_u32_e32 v38, s6, v167
	ds_read_b128 v[34:37], v38 offset:24576
	ds_read_b128 v[38:41], v38 offset:32768
	v_add_u32_e32 v173, s6, v168
	ds_read_b128 v[174:177], v173 offset:24576
	ds_read_b128 v[178:181], v173 offset:32768
	v_add_u32_e32 v173, s6, v166
	s_waitcnt lgkmcnt(3)
	v_mfma_f32_32x32x16_bf16 v[66:81], v[34:37], v[106:109], v[188:203]
	v_exp_f32_e32 v182, v57
	v_exp_f32_e32 v183, v58
	v_exp_f32_e32 v184, v59
	v_add_f32_e32 v143, v222, v227
	s_waitcnt lgkmcnt(2)
	v_mfma_f32_32x32x16_bf16 v[34:49], v[38:41], v[106:109], v[188:203]
	v_exp_f32_e32 v185, v60
	v_exp_f32_e32 v186, v61
	v_exp_f32_e32 v187, v62
	v_add_f32_e32 v145, v223, v230
	s_waitcnt lgkmcnt(1)
	v_mfma_f32_32x32x16_bf16 v[66:81], v[174:177], v[102:105], v[66:81]
	v_exp_f32_e32 v204, v63
	v_exp_f32_e32 v205, v64
	v_exp_f32_e32 v65, v65
	v_add_f32_e32 v143, v231, v143
	s_waitcnt lgkmcnt(0)
	v_mfma_f32_32x32x16_bf16 v[34:49], v[178:181], v[102:105], v[34:49]
	v_exp_f32_e32 v148, v50
	v_exp_f32_e32 v149, v51
	v_exp_f32_e32 v150, v52
	v_add_f32_e32 v145, v232, v145
	ds_read_b128 v[174:177], v173 offset:24576
	ds_read_b128 v[178:181], v173 offset:32768
	v_add_u32_e32 v173, s6, v162
	s_waitcnt lgkmcnt(1)
	v_mfma_f32_32x32x16_bf16 v[66:81], v[174:177], v[98:101], v[66:81]
	v_exp_f32_e32 v151, v53
	v_exp_f32_e32 v152, v54
	v_exp_f32_e32 v147, v55
	v_add_f32_e32 v143, v233, v143
	s_waitcnt lgkmcnt(0)
	v_mfma_f32_32x32x16_bf16 v[34:49], v[178:181], v[98:101], v[34:49]
	v_exp_f32_e32 v153, v56
	v_add_f32_e32 v145, v234, v145
	v_add_f32_e32 v143, v235, v143
	v_add_f32_e32 v145, v236, v145
	v_add_f32_e32 v143, v237, v143
	v_add_f32_e32 v145, v238, v145
	ds_read_b128 v[174:177], v173 offset:24576
	ds_read_b128 v[178:181], v173 offset:32768
	v_add_u32_e32 v173, s6, v161
	s_waitcnt lgkmcnt(1)
	v_mfma_f32_32x32x16_bf16 v[66:81], v[174:177], v[94:97], v[66:81]
	v_add_f32_e32 v143, v239, v143
	v_add_f32_e32 v145, v240, v145
	v_add_f32_e32 v143, v241, v143
	v_add_f32_e32 v145, v246, v145
	v_add_f32_e32 v143, v148, v143
	v_add_f32_e32 v145, v149, v145
	v_add_f32_e32 v143, v150, v143
	s_waitcnt lgkmcnt(0)
	v_mfma_f32_32x32x16_bf16 v[34:49], v[178:181], v[94:97], v[34:49]
	v_add_f32_e32 v145, v151, v145
	v_add_f32_e32 v143, v152, v143
	v_add_f32_e32 v145, v147, v145
	v_add_f32_e32 v143, v153, v143
	v_add_f32_e32 v145, v182, v145
	v_add_f32_e32 v143, v183, v143
	v_add_f32_e32 v145, v184, v145
	ds_read_b128 v[174:177], v173 offset:24576
	ds_read_b128 v[178:181], v173 offset:32768
	v_add_u32_e32 v173, s6, v160
	v_lshl_add_u32 v247, s10, 13, v158
	ds_read_b64_tr_b16 v[206:207], v247 offset:0
	ds_read_b64_tr_b16 v[208:209], v247 offset:0x400
	ds_read_b64_tr_b16 v[210:211], v247 offset:0x800
	ds_read_b64_tr_b16 v[212:213], v247 offset:0xc00
	ds_read_b64_tr_b16 v[214:215], v247 offset:0x1000
	ds_read_b64_tr_b16 v[216:217], v247 offset:0x1400
	ds_read_b64_tr_b16 v[218:219], v247 offset:0x1800
	ds_read_b64_tr_b16 v[220:221], v247 offset:0x1c00
	s_waitcnt lgkmcnt(9)
	v_mfma_f32_32x32x16_bf16 v[66:81], v[174:177], v[90:93], v[66:81]
	v_add_f32_e32 v143, v185, v143
	v_add_f32_e32 v145, v186, v145
	v_add_f32_e32 v143, v187, v143
	v_add_f32_e32 v145, v204, v145
	v_add_f32_e32 v143, v205, v143
	v_add_f32_e32 v145, v65, v145
	v_cvt_pk_bf16_f32 v50, v222, v223
	s_waitcnt lgkmcnt(8)
	v_mfma_f32_32x32x16_bf16 v[34:49], v[178:181], v[90:93], v[34:49]
	v_cvt_pk_bf16_f32 v51, v227, v230
	v_cvt_pk_bf16_f32 v52, v231, v232
	v_cvt_pk_bf16_f32 v53, v233, v234
	v_cvt_pk_bf16_f32 v54, v235, v236
	v_cvt_pk_bf16_f32 v55, v237, v238
	v_cvt_pk_bf16_f32 v56, v239, v240
	v_cvt_pk_bf16_f32 v57, v241, v246
	ds_read_b128 v[174:177], v173 offset:24576
	ds_read_b128 v[178:181], v173 offset:32768
	s_waitcnt lgkmcnt(1)
	v_mfma_f32_32x32x16_bf16 v[66:81], v[174:177], v[86:89], v[66:81]
	v_cvt_pk_bf16_f32 v58, v148, v149
	v_cvt_pk_bf16_f32 v59, v150, v151
	v_cvt_pk_bf16_f32 v60, v152, v147
	v_cvt_pk_bf16_f32 v61, v153, v182
	v_cvt_pk_bf16_f32 v62, v183, v184
	v_cvt_pk_bf16_f32 v63, v185, v186
	v_cvt_pk_bf16_f32 v64, v187, v204
	s_waitcnt lgkmcnt(0)
	v_mfma_f32_32x32x16_bf16 v[34:49], v[178:181], v[86:89], v[34:49]
	v_cvt_pk_bf16_f32 v65, v205, v65
	v_add_f32_e32 v173, v143, v145
	s_cmp_ge_u32 s8, s19
	s_cselect_b64 s[4:5], -1, 0
	s_and_b64 vcc, exec, s[4:5]
	s_cbranch_vccnz .Lattn_h2_noload
	global_load_dwordx4 v[114:117], v146, s[84:85]
	global_load_dwordx4 v[118:121], v144, s[82:83]
	global_load_dwordx4 v[122:125], v142, s[82:83]
	s_add_u32 s82, s82, 0x3000
	s_addc_u32 s83, s83, 0
	s_add_u32 s84, s84, 0x2000
	s_addc_u32 s85, s85, 0
.LBB0_1439:
	s_waitcnt lgkmcnt(0)
	s_nop 0
	v_mfma_f32_32x32x16_bf16 v[2:17], v[50:53], v[206:209], v[2:17]
	ds_read_b64_tr_b16 v[148:149], v247 offset:0x200
	ds_read_b64_tr_b16 v[150:151], v247 offset:0x600
	v_max_f32_e32 v249, v67, v67
	v_max_f32_e32 v248, v66, v66
	v_max_f32_e32 v248, v248, v249
	v_max3_f32 v248, v248, v68, v69
	v_exp_f32_e32 v222, v66
	v_mfma_f32_32x32x16_bf16 v[2:17], v[54:57], v[210:213], v[2:17]
	ds_read_b64_tr_b16 v[176:177], v247 offset:0xa00
	ds_read_b64_tr_b16 v[178:179], v247 offset:0xe00
	v_max3_f32 v248, v248, v70, v71
	v_max3_f32 v248, v248, v72, v73
	v_max3_f32 v248, v248, v74, v75
	v_exp_f32_e32 v223, v67
	v_exp_f32_e32 v227, v68
	v_mfma_f32_32x32x16_bf16 v[2:17], v[58:61], v[214:217], v[2:17]
	ds_read_b64_tr_b16 v[180:181], v247 offset:0x1200
	ds_read_b64_tr_b16 v[182:183], v247 offset:0x1600
	v_max3_f32 v248, v248, v76, v77
	v_max3_f32 v248, v248, v78, v79
	v_max3_f32 v248, v248, v80, v81
	v_exp_f32_e32 v230, v69
	v_exp_f32_e32 v231, v70
	v_mfma_f32_32x32x16_bf16 v[2:17], v[62:65], v[218:221], v[2:17]
	ds_read_b64_tr_b16 v[184:185], v247 offset:0x1a00
	ds_read_b64_tr_b16 v[186:187], v247 offset:0x1e00
	v_max3_f32 v248, v248, v34, v35
	v_max3_f32 v248, v248, v36, v37
	v_max3_f32 v248, v248, v38, v39
	v_exp_f32_e32 v232, v71
	v_exp_f32_e32 v233, v72
	s_add_i32 s6, s9, 1
	s_cmp_lg_u32 s9, 2
	s_cselect_b32 s10, s6, 0
	s_lshl_b32 s20, s10, 13
	s_lshl_b32 s6, s10, 14
	s_add_i32 s21, s6, 0
	s_waitcnt vmcnt(3)
	v_add_u32_e32 v247, s20, v165
	ds_write_b128 v247, v[130:133]
	v_add_u32_e32 v247, s21, v163
	ds_write_b128 v247, v[126:129] offset:24576
	v_add_u32_e32 v247, s21, v164
	ds_write_b128 v247, v[134:137] offset:24576
	s_waitcnt lgkmcnt(3)
	v_mfma_f32_32x32x16_bf16 v[18:33], v[50:53], v[148:151], v[18:33]
	v_max3_f32 v248, v248, v40, v41
	v_max3_f32 v248, v248, v42, v43
	v_max3_f32 v248, v248, v44, v45
	v_exp_f32_e32 v234, v73
	v_exp_f32_e32 v235, v74
	v_mfma_f32_32x32x16_bf16 v[18:33], v[54:57], v[176:179], v[18:33]
	v_max3_f32 v248, v248, v46, v47
	v_max3_f32 v248, v248, v48, v49
	v_exp_f32_e32 v236, v75
	v_exp_f32_e32 v237, v76
	v_exp_f32_e32 v238, v77
	v_mfma_f32_32x32x16_bf16 v[18:33], v[58:61], v[180:183], v[18:33]
	v_exp_f32_e32 v239, v78
	v_exp_f32_e32 v240, v79
	v_exp_f32_e32 v241, v80
	v_exp_f32_e32 v246, v81
	s_mov_b32 s6, 0x41380000
	v_cmp_ge_f32_e32 vcc, s6, v248
	v_mfma_f32_32x32x16_bf16 v[18:33], v[62:65], v[184:187], v[18:33]
	s_cmp_eq_u64 vcc, exec
	v_mov_b32_e32 v148, 1.0
	s_cbranch_scc0 .LBB0_1449

.LBB0_1448:
	v_mov_b32_e32 v249, v248
	s_nop 1
	v_permlane32_swap_b32_e32 v248, v249
	v_max_f32_e32 v249, v249, v249
	v_max_f32_e32 v248, v248, v248
	v_max_f32_e32 v34, v248, v249
	v_max_f32_e32 v34, v34, v34
	v_max_f32_e32 v34, 0, v34
	v_add_f32_e32 v34, v159, v34
	v_cvt_pk_bf16_f32 v34, v34, v83
	s_nop 0
	v_lshlrev_b32_e32 v35, 16, v34
	v_sub_f32_e32 v34, v35, v159
	v_exp_f32_e64 v172, -v34
	v_pk_add_f32 v[66:67], v[66:67], v[34:35] op_sel_hi:[1,0] neg_lo:[0,1] neg_hi:[0,1]
	v_pk_add_f32 v[68:69], v[68:69], v[34:35] op_sel_hi:[1,0] neg_lo:[0,1] neg_hi:[0,1]
	v_pk_add_f32 v[70:71], v[70:71], v[34:35] op_sel_hi:[1,0] neg_lo:[0,1] neg_hi:[0,1]
	v_pk_add_f32 v[72:73], v[72:73], v[34:35] op_sel_hi:[1,0] neg_lo:[0,1] neg_hi:[0,1]
	v_pk_add_f32 v[74:75], v[74:75], v[34:35] op_sel_hi:[1,0] neg_lo:[0,1] neg_hi:[0,1]
	v_pk_add_f32 v[76:77], v[76:77], v[34:35] op_sel_hi:[1,0] neg_lo:[0,1] neg_hi:[0,1]
	v_pk_add_f32 v[78:79], v[78:79], v[34:35] op_sel_hi:[1,0] neg_lo:[0,1] neg_hi:[0,1]
	v_pk_add_f32 v[80:81], v[80:81], v[34:35] op_sel_hi:[1,0] neg_lo:[0,1] neg_hi:[0,1]
	v_sub_f32_e32 v65, v65, v34
	v_sub_f32_e32 v64, v64, v34
	v_sub_f32_e32 v63, v63, v34
	v_sub_f32_e32 v62, v62, v34
	v_sub_f32_e32 v61, v61, v34
	v_sub_f32_e32 v60, v60, v34
	v_sub_f32_e32 v59, v59, v34
	v_sub_f32_e32 v58, v58, v34
	v_sub_f32_e32 v57, v57, v34
	v_sub_f32_e32 v56, v56, v34
	v_sub_f32_e32 v55, v55, v34
	v_sub_f32_e32 v54, v54, v34
	v_sub_f32_e32 v53, v53, v34
	v_sub_f32_e32 v52, v52, v34
	v_sub_f32_e32 v51, v51, v34
	v_sub_f32_e32 v50, v50, v34
	v_exp_f32_e32 v222, v66
	v_exp_f32_e32 v223, v67
	v_exp_f32_e32 v227, v68
	v_exp_f32_e32 v230, v69
	v_exp_f32_e32 v231, v70
	v_exp_f32_e32 v232, v71
	v_exp_f32_e32 v233, v72
	v_exp_f32_e32 v234, v73
	v_exp_f32_e32 v235, v74
	v_exp_f32_e32 v236, v75
	v_exp_f32_e32 v237, v76
	v_exp_f32_e32 v238, v77
	v_exp_f32_e32 v239, v78
	v_exp_f32_e32 v240, v79
	v_exp_f32_e32 v241, v80
	v_exp_f32_e32 v246, v81
	v_mov_b32_e32 v159, v35
	v_xor_b32_e32 v188, 0x80000000, v35
	v_xor_b32_e32 v189, 0x80000000, v35
	v_xor_b32_e32 v190, 0x80000000, v35
	v_xor_b32_e32 v191, 0x80000000, v35
	v_xor_b32_e32 v192, 0x80000000, v35
	v_xor_b32_e32 v193, 0x80000000, v35
	v_xor_b32_e32 v194, 0x80000000, v35
	v_xor_b32_e32 v195, 0x80000000, v35
	v_xor_b32_e32 v196, 0x80000000, v35
	v_xor_b32_e32 v197, 0x80000000, v35
	v_xor_b32_e32 v198, 0x80000000, v35
	v_xor_b32_e32 v199, 0x80000000, v35
	v_xor_b32_e32 v200, 0x80000000, v35
	v_xor_b32_e32 v201, 0x80000000, v35
	v_xor_b32_e32 v202, 0x80000000, v35
	v_xor_b32_e32 v203, 0x80000000, v35
	s_branch .LBB0_1431
.LBB0_1449:
	v_mov_b32_e32 v249, v248
	s_nop 1
	v_permlane32_swap_b32_e32 v248, v249
	v_max_f32_e32 v249, v249, v249
	v_max_f32_e32 v248, v248, v248
	v_max_f32_e32 v50, v248, v249
	v_max_f32_e32 v50, v50, v50
	v_max_f32_e32 v50, 0, v50
	v_add_f32_e32 v50, v159, v50
	v_cvt_pk_bf16_f32 v50, v50, v83
	s_nop 0
	v_lshlrev_b32_e32 v51, 16, v50
	v_sub_f32_e32 v50, v51, v159
	v_exp_f32_e64 v148, -v50
	v_pk_add_f32 v[66:67], v[66:67], v[50:51] op_sel_hi:[1,0] neg_lo:[0,1] neg_hi:[0,1]
	v_pk_add_f32 v[68:69], v[68:69], v[50:51] op_sel_hi:[1,0] neg_lo:[0,1] neg_hi:[0,1]
	v_pk_add_f32 v[70:71], v[70:71], v[50:51] op_sel_hi:[1,0] neg_lo:[0,1] neg_hi:[0,1]
	v_pk_add_f32 v[72:73], v[72:73], v[50:51] op_sel_hi:[1,0] neg_lo:[0,1] neg_hi:[0,1]
	v_pk_add_f32 v[74:75], v[74:75], v[50:51] op_sel_hi:[1,0] neg_lo:[0,1] neg_hi:[0,1]
	v_pk_add_f32 v[76:77], v[76:77], v[50:51] op_sel_hi:[1,0] neg_lo:[0,1] neg_hi:[0,1]
	v_pk_add_f32 v[78:79], v[78:79], v[50:51] op_sel_hi:[1,0] neg_lo:[0,1] neg_hi:[0,1]
	v_pk_add_f32 v[80:81], v[80:81], v[50:51] op_sel_hi:[1,0] neg_lo:[0,1] neg_hi:[0,1]
	v_sub_f32_e32 v49, v49, v50
	v_sub_f32_e32 v48, v48, v50
	v_sub_f32_e32 v47, v47, v50
	v_sub_f32_e32 v46, v46, v50
	v_sub_f32_e32 v45, v45, v50
	v_sub_f32_e32 v44, v44, v50
	v_sub_f32_e32 v43, v43, v50
	v_sub_f32_e32 v42, v42, v50
	v_sub_f32_e32 v41, v41, v50
	v_sub_f32_e32 v40, v40, v50
	v_sub_f32_e32 v39, v39, v50
	v_sub_f32_e32 v38, v38, v50
	v_sub_f32_e32 v37, v37, v50
	v_sub_f32_e32 v36, v36, v50
	v_sub_f32_e32 v35, v35, v50
	v_sub_f32_e32 v34, v34, v50
	v_exp_f32_e32 v222, v66
	v_exp_f32_e32 v223, v67
	v_exp_f32_e32 v227, v68
	v_exp_f32_e32 v230, v69
	v_exp_f32_e32 v231, v70
	v_exp_f32_e32 v232, v71
	v_exp_f32_e32 v233, v72
	v_exp_f32_e32 v234, v73
	v_exp_f32_e32 v235, v74
	v_exp_f32_e32 v236, v75
	v_exp_f32_e32 v237, v76
	v_exp_f32_e32 v238, v77
	v_exp_f32_e32 v239, v78
	v_exp_f32_e32 v240, v79
	v_exp_f32_e32 v241, v80
	v_exp_f32_e32 v246, v81
	v_mov_b32_e32 v159, v51
	v_xor_b32_e32 v188, 0x80000000, v51
	v_xor_b32_e32 v189, 0x80000000, v51
	v_xor_b32_e32 v190, 0x80000000, v51
	v_xor_b32_e32 v191, 0x80000000, v51
	v_xor_b32_e32 v192, 0x80000000, v51
	v_xor_b32_e32 v193, 0x80000000, v51
	v_xor_b32_e32 v194, 0x80000000, v51
	v_xor_b32_e32 v195, 0x80000000, v51
	v_xor_b32_e32 v196, 0x80000000, v51
	v_xor_b32_e32 v197, 0x80000000, v51
	v_xor_b32_e32 v198, 0x80000000, v51
	v_xor_b32_e32 v199, 0x80000000, v51
	v_xor_b32_e32 v200, 0x80000000, v51
	v_xor_b32_e32 v201, 0x80000000, v51
	v_xor_b32_e32 v202, 0x80000000, v51
	v_xor_b32_e32 v203, 0x80000000, v51
	s_branch .LBB0_1440

.LBB0_1542:
	v_add_u32_e32 v82, s67, v160
	ds_read_b128 v[132:135], v82
	ds_read_b128 v[144:147], v82 offset:1024
	ds_read_b128 v[148:151], v82 offset:2048
	ds_read_b128 v[168:171], v82 offset:3072
	s_add_u32 s24, s22, 0x100
	s_addc_u32 s25, s23, 0
	s_cmp_eq_u32 s51, 12
	s_cselect_b32 s29, s19, s25
	s_cselect_b32 s28, s48, s24
	s_cselect_b32 s27, s21, s50
	s_cselect_b32 s26, s20, s49
	v_add_u32_e32 v82, 0xc000, v154
	v_lshl_add_u64 v[204:205], s[22:23], 0, v[140:141]
	v_readfirstlane_b32 s52, v82
	s_mov_b32 m0, s52
	v_add_u32_e32 v82, 0xe000, v154
	ds_read_b128 v[172:175], v167
	ds_read_b128 v[176:179], v167 offset:1024
	ds_read_b128 v[180:183], v167 offset:2048
	ds_read_b128 v[184:187], v167 offset:3072
	ds_read_b128 v[188:191], v167 offset:4096
	ds_read_b128 v[192:195], v167 offset:5120
	ds_read_b128 v[196:199], v167 offset:6144
	ds_read_b128 v[200:203], v167 offset:7168
	global_load_lds_dwordx4 v[204:205], off
	v_lshl_add_u64 v[204:205], s[22:23], 0, v[142:143]
	v_readfirstlane_b32 s22, v82
	s_mov_b32 m0, s22
	s_nop 0
	global_load_lds_dwordx4 v[204:205], off
	s_waitcnt lgkmcnt(8)
	s_barrier
	s_waitcnt lgkmcnt(0)
	s_setprio 1
	s_waitcnt lgkmcnt(0)
	v_mfma_f32_16x16x32_bf16 v[128:131], v[132:135], v[172:175], v[128:131]
	v_mfma_f32_16x16x32_bf16 v[100:103], v[148:151], v[172:175], v[100:103]
	v_mfma_f32_16x16x32_bf16 v[124:127], v[132:135], v[180:183], v[124:127]
	v_mfma_f32_16x16x32_bf16 v[96:99], v[148:151], v[180:183], v[96:99]
	v_mfma_f32_16x16x32_bf16 v[120:123], v[132:135], v[188:191], v[120:123]
	v_mfma_f32_16x16x32_bf16 v[88:91], v[148:151], v[188:191], v[88:91]
	v_mfma_f32_16x16x32_bf16 v[116:119], v[132:135], v[196:199], v[116:119]
	v_mfma_f32_16x16x32_bf16 v[84:87], v[148:151], v[196:199], v[84:87]
	v_mfma_f32_16x16x32_bf16 v[128:131], v[144:147], v[176:179], v[128:131]
	v_mfma_f32_16x16x32_bf16 v[100:103], v[168:171], v[176:179], v[100:103]
	v_mfma_f32_16x16x32_bf16 v[124:127], v[144:147], v[184:187], v[124:127]
	v_mfma_f32_16x16x32_bf16 v[96:99], v[168:171], v[184:187], v[96:99]
	v_mfma_f32_16x16x32_bf16 v[120:123], v[144:147], v[192:195], v[120:123]
	v_mfma_f32_16x16x32_bf16 v[88:91], v[168:171], v[192:195], v[88:91]
	v_mfma_f32_16x16x32_bf16 v[116:119], v[144:147], v[200:203], v[116:119]
	v_mfma_f32_16x16x32_bf16 v[84:87], v[168:171], v[200:203], v[84:87]
	s_setprio 0
	s_barrier
	v_readfirstlane_b32 s22, v152
	v_add_u32_e32 v82, s68, v160
	v_lshl_add_u64 v[220:221], s[26:27], 0, v[136:137]
	s_mov_b32 m0, s22
	v_readfirstlane_b32 s22, v153
	ds_read_b128 v[204:207], v82
	ds_read_b128 v[208:211], v82 offset:1024
	ds_read_b128 v[212:215], v82 offset:2048
	ds_read_b128 v[216:219], v82 offset:3072
	global_load_lds_dwordx4 v[220:221], off
	v_lshl_add_u64 v[222:223], s[26:27], 0, v[138:139]
	s_mov_b32 m0, s22
	s_nop 0
	global_load_lds_dwordx4 v[222:223], off
	s_barrier
	s_waitcnt lgkmcnt(0)
	s_setprio 1
	s_waitcnt lgkmcnt(0)
	v_mfma_f32_16x16x32_bf16 v[66:69], v[204:207], v[172:175], v[66:69]
	v_mfma_f32_16x16x32_bf16 v[38:41], v[212:215], v[172:175], v[38:41]
	v_mfma_f32_16x16x32_bf16 v[58:61], v[204:207], v[180:183], v[58:61]
	v_mfma_f32_16x16x32_bf16 v[30:33], v[212:215], v[180:183], v[30:33]
	v_mfma_f32_16x16x32_bf16 v[54:57], v[204:207], v[188:191], v[54:57]
	v_mfma_f32_16x16x32_bf16 v[22:25], v[212:215], v[188:191], v[22:25]
	v_mfma_f32_16x16x32_bf16 v[50:53], v[204:207], v[196:199], v[50:53]
	v_mfma_f32_16x16x32_bf16 v[18:21], v[212:215], v[196:199], v[18:21]
	v_mfma_f32_16x16x32_bf16 v[66:69], v[208:211], v[176:179], v[66:69]
	v_mfma_f32_16x16x32_bf16 v[38:41], v[216:219], v[176:179], v[38:41]
	v_mfma_f32_16x16x32_bf16 v[58:61], v[208:211], v[184:187], v[58:61]
	v_mfma_f32_16x16x32_bf16 v[30:33], v[216:219], v[184:187], v[30:33]
	v_mfma_f32_16x16x32_bf16 v[54:57], v[208:211], v[192:195], v[54:57]
	v_mfma_f32_16x16x32_bf16 v[22:25], v[216:219], v[192:195], v[22:25]
	v_mfma_f32_16x16x32_bf16 v[50:53], v[208:211], v[200:203], v[50:53]
	v_mfma_f32_16x16x32_bf16 v[18:21], v[216:219], v[200:203], v[18:21]
	s_setprio 0
	v_readfirstlane_b32 s22, v154
	v_lshl_add_u64 v[230:231], s[28:29], 0, v[136:137]
	s_mov_b32 m0, s22
	v_readfirstlane_b32 s22, v155
	s_barrier
	ds_read_b128 v[172:175], v167 offset:16384
	ds_read_b128 v[176:179], v167 offset:17408
	ds_read_b128 v[180:183], v167 offset:18432
	ds_read_b128 v[184:187], v167 offset:19456
	ds_read_b128 v[188:191], v167 offset:20480
	ds_read_b128 v[192:195], v167 offset:21504
	ds_read_b128 v[196:199], v167 offset:22528
	ds_read_b128 v[200:203], v167 offset:23552
	global_load_lds_dwordx4 v[230:231], off
	v_lshl_add_u64 v[232:233], s[28:29], 0, v[138:139]
	s_mov_b32 m0, s22
	s_nop 0
	global_load_lds_dwordx4 v[232:233], off
	s_barrier
	s_waitcnt lgkmcnt(0)
	s_setprio 1
	s_waitcnt lgkmcnt(0)
	v_mfma_f32_16x16x32_bf16 v[112:115], v[132:135], v[172:175], v[112:115]
	v_mfma_f32_16x16x32_bf16 v[78:81], v[148:151], v[172:175], v[78:81]
	v_mfma_f32_16x16x32_bf16 v[108:111], v[132:135], v[180:183], v[108:111]
	v_mfma_f32_16x16x32_bf16 v[74:77], v[148:151], v[180:183], v[74:77]
	v_mfma_f32_16x16x32_bf16 v[104:107], v[132:135], v[188:191], v[104:107]
	v_mfma_f32_16x16x32_bf16 v[70:73], v[148:151], v[188:191], v[70:73]
	v_mfma_f32_16x16x32_bf16 v[92:95], v[132:135], v[196:199], v[92:95]
	v_mfma_f32_16x16x32_bf16 v[62:65], v[148:151], v[196:199], v[62:65]
	v_mfma_f32_16x16x32_bf16 v[112:115], v[144:147], v[176:179], v[112:115]
	v_mfma_f32_16x16x32_bf16 v[78:81], v[168:171], v[176:179], v[78:81]
	v_mfma_f32_16x16x32_bf16 v[108:111], v[144:147], v[184:187], v[108:111]
	v_mfma_f32_16x16x32_bf16 v[74:77], v[168:171], v[184:187], v[74:77]
	v_mfma_f32_16x16x32_bf16 v[104:107], v[144:147], v[192:195], v[104:107]
	v_mfma_f32_16x16x32_bf16 v[70:73], v[168:171], v[192:195], v[70:73]
	v_mfma_f32_16x16x32_bf16 v[92:95], v[144:147], v[200:203], v[92:95]
	v_mfma_f32_16x16x32_bf16 v[62:65], v[168:171], v[200:203], v[62:65]
	s_setprio 0
	s_barrier
	s_add_u32 s22, s26, 0x40000
	s_addc_u32 s23, s27, 0
	v_readfirstlane_b32 s52, v156
	v_lshl_add_u64 v[132:133], s[22:23], 0, v[136:137]
	s_mov_b32 m0, s52
	s_nop 0
	global_load_lds_dwordx4 v[132:133], off
	v_lshl_add_u64 v[132:133], s[22:23], 0, v[138:139]
	v_readfirstlane_b32 s22, v157
	s_mov_b32 m0, s22
	s_nop 0
	global_load_lds_dwordx4 v[132:133], off
	s_waitcnt vmcnt(6)
	s_barrier
	s_setprio 1
	v_mfma_f32_16x16x32_bf16 v[46:49], v[204:207], v[172:175], v[46:49]
	v_mfma_f32_16x16x32_bf16 v[14:17], v[212:215], v[172:175], v[14:17]
	v_mfma_f32_16x16x32_bf16 v[42:45], v[204:207], v[180:183], v[42:45]
	v_mfma_f32_16x16x32_bf16 v[10:13], v[212:215], v[180:183], v[10:13]
	v_mfma_f32_16x16x32_bf16 v[34:37], v[204:207], v[188:191], v[34:37]
	v_mfma_f32_16x16x32_bf16 v[6:9], v[212:215], v[188:191], v[6:9]
	v_mfma_f32_16x16x32_bf16 v[26:29], v[204:207], v[196:199], v[26:29]
	v_mfma_f32_16x16x32_bf16 v[2:5], v[212:215], v[196:199], v[2:5]
	v_mfma_f32_16x16x32_bf16 v[46:49], v[208:211], v[176:179], v[46:49]
	v_mfma_f32_16x16x32_bf16 v[14:17], v[216:219], v[176:179], v[14:17]
	v_mfma_f32_16x16x32_bf16 v[42:45], v[208:211], v[184:187], v[42:45]
	v_mfma_f32_16x16x32_bf16 v[10:13], v[216:219], v[184:187], v[10:13]
	v_mfma_f32_16x16x32_bf16 v[34:37], v[208:211], v[192:195], v[34:37]
	v_mfma_f32_16x16x32_bf16 v[6:9], v[216:219], v[192:195], v[6:9]
	v_mfma_f32_16x16x32_bf16 v[26:29], v[208:211], v[200:203], v[26:29]
	v_mfma_f32_16x16x32_bf16 v[2:5], v[216:219], v[200:203], v[2:5]
	s_setprio 0
	v_add_u32_e32 v82, s70, v160
	s_barrier
	ds_read_b128 v[132:135], v82
	ds_read_b128 v[144:147], v82 offset:1024
	ds_read_b128 v[148:151], v82 offset:2048
	ds_read_b128 v[168:171], v82 offset:3072
	s_add_u32 s22, s28, 0x40000
	s_addc_u32 s23, s29, 0
	v_readfirstlane_b32 s28, v158
	v_lshl_add_u64 v[204:205], s[22:23], 0, v[136:137]
	s_mov_b32 m0, s28
	ds_read_b128 v[172:175], v167 offset:32768
	ds_read_b128 v[176:179], v167 offset:33792
	ds_read_b128 v[180:183], v167 offset:34816
	ds_read_b128 v[184:187], v167 offset:35840
	ds_read_b128 v[188:191], v167 offset:36864
	ds_read_b128 v[192:195], v167 offset:37888
	ds_read_b128 v[196:199], v167 offset:38912
	ds_read_b128 v[200:203], v167 offset:39936
	global_load_lds_dwordx4 v[204:205], off
	v_lshl_add_u64 v[204:205], s[22:23], 0, v[138:139]
	v_readfirstlane_b32 s22, v159
	s_mov_b32 m0, s22
	s_nop 0
	global_load_lds_dwordx4 v[204:205], off
	s_waitcnt lgkmcnt(8)
	s_barrier
	s_waitcnt lgkmcnt(0)
	s_setprio 1
	s_waitcnt lgkmcnt(0)
	v_mfma_f32_16x16x32_bf16 v[128:131], v[132:135], v[172:175], v[128:131]
	v_mfma_f32_16x16x32_bf16 v[100:103], v[148:151], v[172:175], v[100:103]
	v_mfma_f32_16x16x32_bf16 v[124:127], v[132:135], v[180:183], v[124:127]
	v_mfma_f32_16x16x32_bf16 v[96:99], v[148:151], v[180:183], v[96:99]
	v_mfma_f32_16x16x32_bf16 v[120:123], v[132:135], v[188:191], v[120:123]
	v_mfma_f32_16x16x32_bf16 v[88:91], v[148:151], v[188:191], v[88:91]
	v_mfma_f32_16x16x32_bf16 v[116:119], v[132:135], v[196:199], v[116:119]
	v_mfma_f32_16x16x32_bf16 v[84:87], v[148:151], v[196:199], v[84:87]
	v_mfma_f32_16x16x32_bf16 v[128:131], v[144:147], v[176:179], v[128:131]
	v_mfma_f32_16x16x32_bf16 v[100:103], v[168:171], v[176:179], v[100:103]
	v_mfma_f32_16x16x32_bf16 v[124:127], v[144:147], v[184:187], v[124:127]
	v_mfma_f32_16x16x32_bf16 v[96:99], v[168:171], v[184:187], v[96:99]
	v_mfma_f32_16x16x32_bf16 v[120:123], v[144:147], v[192:195], v[120:123]
	v_mfma_f32_16x16x32_bf16 v[88:91], v[168:171], v[192:195], v[88:91]
	v_mfma_f32_16x16x32_bf16 v[116:119], v[144:147], v[200:203], v[116:119]
	v_mfma_f32_16x16x32_bf16 v[84:87], v[168:171], v[200:203], v[84:87]
	s_setprio 0
	s_barrier
	v_readfirstlane_b32 s22, v161
	v_add_u32_e32 v82, s71, v160
	v_lshl_add_u64 v[220:221], v[220:221], 0, s[54:55]
	s_mov_b32 m0, s22
	v_readfirstlane_b32 s22, v162
	ds_read_b128 v[204:207], v82
	ds_read_b128 v[208:211], v82 offset:1024
	ds_read_b128 v[212:215], v82 offset:2048
	ds_read_b128 v[216:219], v82 offset:3072
	global_load_lds_dwordx4 v[220:221], off
	v_lshl_add_u64 v[220:221], v[222:223], 0, s[54:55]
	s_mov_b32 m0, s22
	s_nop 0
	global_load_lds_dwordx4 v[220:221], off
	s_barrier
	s_waitcnt lgkmcnt(0)
	s_setprio 1
	s_waitcnt lgkmcnt(0)
	v_mfma_f32_16x16x32_bf16 v[66:69], v[204:207], v[172:175], v[66:69]
	v_mfma_f32_16x16x32_bf16 v[38:41], v[212:215], v[172:175], v[38:41]
	v_mfma_f32_16x16x32_bf16 v[58:61], v[204:207], v[180:183], v[58:61]
	v_mfma_f32_16x16x32_bf16 v[30:33], v[212:215], v[180:183], v[30:33]
	v_mfma_f32_16x16x32_bf16 v[54:57], v[204:207], v[188:191], v[54:57]
	v_mfma_f32_16x16x32_bf16 v[22:25], v[212:215], v[188:191], v[22:25]
	v_mfma_f32_16x16x32_bf16 v[50:53], v[204:207], v[196:199], v[50:53]
	v_mfma_f32_16x16x32_bf16 v[18:21], v[212:215], v[196:199], v[18:21]
	v_mfma_f32_16x16x32_bf16 v[66:69], v[208:211], v[176:179], v[66:69]
	v_mfma_f32_16x16x32_bf16 v[38:41], v[216:219], v[176:179], v[38:41]
	v_mfma_f32_16x16x32_bf16 v[58:61], v[208:211], v[184:187], v[58:61]
	v_mfma_f32_16x16x32_bf16 v[30:33], v[216:219], v[184:187], v[30:33]
	v_mfma_f32_16x16x32_bf16 v[54:57], v[208:211], v[192:195], v[54:57]
	v_mfma_f32_16x16x32_bf16 v[22:25], v[216:219], v[192:195], v[22:25]
	v_mfma_f32_16x16x32_bf16 v[50:53], v[208:211], v[200:203], v[50:53]
	v_mfma_f32_16x16x32_bf16 v[18:21], v[216:219], v[200:203], v[18:21]
	s_setprio 0
	v_readfirstlane_b32 s22, v163
	v_lshl_add_u64 v[220:221], v[230:231], 0, s[54:55]
	s_mov_b32 m0, s22
	v_readfirstlane_b32 s22, v164
	s_barrier
	ds_read_b128 v[172:175], v167 offset:49152
	ds_read_b128 v[176:179], v167 offset:50176
	ds_read_b128 v[180:183], v167 offset:51200
	ds_read_b128 v[184:187], v167 offset:52224
	ds_read_b128 v[188:191], v167 offset:53248
	ds_read_b128 v[192:195], v167 offset:54272
	ds_read_b128 v[196:199], v167 offset:55296
	ds_read_b128 v[200:203], v167 offset:56320
	global_load_lds_dwordx4 v[220:221], off
	v_lshl_add_u64 v[220:221], v[232:233], 0, s[54:55]
	s_mov_b32 m0, s22
	s_nop 0
	global_load_lds_dwordx4 v[220:221], off
	s_barrier
	s_waitcnt lgkmcnt(0)
	s_setprio 1
	s_waitcnt lgkmcnt(0)
	v_mfma_f32_16x16x32_bf16 v[112:115], v[132:135], v[172:175], v[112:115]
	v_mfma_f32_16x16x32_bf16 v[78:81], v[148:151], v[172:175], v[78:81]
	v_mfma_f32_16x16x32_bf16 v[108:111], v[132:135], v[180:183], v[108:111]
	v_mfma_f32_16x16x32_bf16 v[74:77], v[148:151], v[180:183], v[74:77]
	v_mfma_f32_16x16x32_bf16 v[104:107], v[132:135], v[188:191], v[104:107]
	v_mfma_f32_16x16x32_bf16 v[70:73], v[148:151], v[188:191], v[70:73]
	v_mfma_f32_16x16x32_bf16 v[92:95], v[132:135], v[196:199], v[92:95]
	v_mfma_f32_16x16x32_bf16 v[62:65], v[148:151], v[196:199], v[62:65]
	v_mfma_f32_16x16x32_bf16 v[112:115], v[144:147], v[176:179], v[112:115]
	v_mfma_f32_16x16x32_bf16 v[78:81], v[168:171], v[176:179], v[78:81]
	v_mfma_f32_16x16x32_bf16 v[108:111], v[144:147], v[184:187], v[108:111]
	v_mfma_f32_16x16x32_bf16 v[74:77], v[168:171], v[184:187], v[74:77]
	v_mfma_f32_16x16x32_bf16 v[104:107], v[144:147], v[192:195], v[104:107]
	v_mfma_f32_16x16x32_bf16 v[70:73], v[168:171], v[192:195], v[70:73]
	v_mfma_f32_16x16x32_bf16 v[92:95], v[144:147], v[200:203], v[92:95]
	v_mfma_f32_16x16x32_bf16 v[62:65], v[168:171], v[200:203], v[62:65]
	s_setprio 0
	s_barrier
	s_add_u32 s22, s26, 0x40080
	s_addc_u32 s23, s27, 0
	v_readfirstlane_b32 s26, v165
	v_lshl_add_u64 v[132:133], s[22:23], 0, v[136:137]
	s_mov_b32 m0, s26
	s_nop 0
	global_load_lds_dwordx4 v[132:133], off
	v_lshl_add_u64 v[132:133], s[22:23], 0, v[138:139]
	v_readfirstlane_b32 s22, v166
	s_mov_b32 m0, s22
	s_nop 0
	global_load_lds_dwordx4 v[132:133], off
	s_waitcnt vmcnt(6)
	s_barrier
	s_setprio 1
	v_mfma_f32_16x16x32_bf16 v[46:49], v[204:207], v[172:175], v[46:49]
	v_mfma_f32_16x16x32_bf16 v[14:17], v[212:215], v[172:175], v[14:17]
	v_mfma_f32_16x16x32_bf16 v[42:45], v[204:207], v[180:183], v[42:45]
	v_mfma_f32_16x16x32_bf16 v[10:13], v[212:215], v[180:183], v[10:13]
	v_mfma_f32_16x16x32_bf16 v[34:37], v[204:207], v[188:191], v[34:37]
	v_mfma_f32_16x16x32_bf16 v[6:9], v[212:215], v[188:191], v[6:9]
	v_mfma_f32_16x16x32_bf16 v[26:29], v[204:207], v[196:199], v[26:29]
	v_mfma_f32_16x16x32_bf16 v[2:5], v[212:215], v[196:199], v[2:5]
	v_mfma_f32_16x16x32_bf16 v[46:49], v[208:211], v[176:179], v[46:49]
	v_mfma_f32_16x16x32_bf16 v[14:17], v[216:219], v[176:179], v[14:17]
	v_mfma_f32_16x16x32_bf16 v[42:45], v[208:211], v[184:187], v[42:45]
	v_mfma_f32_16x16x32_bf16 v[10:13], v[216:219], v[184:187], v[10:13]
	v_mfma_f32_16x16x32_bf16 v[34:37], v[208:211], v[192:195], v[34:37]
	v_mfma_f32_16x16x32_bf16 v[6:9], v[216:219], v[192:195], v[6:9]
	v_mfma_f32_16x16x32_bf16 v[26:29], v[208:211], v[200:203], v[26:29]
	v_mfma_f32_16x16x32_bf16 v[2:5], v[216:219], v[200:203], v[2:5]
	s_setprio 0
	s_add_i32 s51, s51, 2
	s_add_u32 s49, s49, 0x100
	s_addc_u32 s50, s50, 0
	s_cmp_gt_u32 s51, 13
	s_mov_b64 s[22:23], s[24:25]
	s_barrier
	s_cbranch_scc0 .LBB0_1542
	s_min_i32 s19, s47, 0x8000
	s_ashr_i32 s19, s19, 14
	s_mul_i32 s20, s19, 0x1800
	s_ashr_i32 s21, s20, 31
	s_lshl_b64 s[20:21], s[20:21], 2
	s_add_u32 s22, s42, s20
	v_mov_b32_e32 v134, v0
	s_addc_u32 s23, s43, s21
	s_ashr_i32 s19, s18, 31
	s_lshl_b64 s[20:21], s[18:19], 2
	v_lshrrev_b32_e32 v82, 1, v134
	s_add_u32 s20, s22, s20
	v_and_b32_e32 v150, 0x60, v82
	s_addc_u32 s21, s23, s21
	v_lshlrev_b32_e32 v82, 2, v150
	v_lshl_add_u64 v[132:133], s[20:21], 0, v[82:83]
	v_lshrrev_b32_e32 v82, 2, v134
	v_and_b32_e32 v151, 12, v82
	v_lshlrev_b32_e32 v82, 2, v151
	v_and_b32_e32 v135, 15, v134
	v_lshl_add_u64 v[146:147], v[132:133], 0, v[82:83]
	v_ashrrev_i32_e32 v82, 2, v134
	s_movk_i32 s20, 0xffc0
	v_and_or_b32 v82, v82, s20, v135
	v_add_u32_e32 v148, s47, v82
	v_ashrrev_i32_e32 v149, 31, v148
	v_lshlrev_b64 v[144:145], 11, v[148:149]
	v_lshl_add_u64 v[144:145], s[8:9], 0, v[144:145]
	s_lshl_b64 s[18:19], s[18:19], 1
	v_lshl_add_u64 v[144:145], v[144:145], 0, s[18:19]
	v_lshlrev_b32_e32 v82, 1, v150
	v_lshl_add_u64 v[144:145], v[144:145], 0, v[82:83]
	v_lshlrev_b32_e32 v150, 1, v151
	v_mov_b32_e32 v151, v83
	v_lshl_add_u64 v[144:145], v[144:145], 0, v[150:151]
	s_mov_b64 s[20:21], 0x8000
	v_lshl_add_u64 v[168:169], v[144:145], 0, s[20:21]
	s_mov_b64 s[20:21], 0x10000
	v_lshl_add_u64 v[172:173], v[144:145], 0, s[20:21]
	s_mov_b64 s[20:21], 0x18000
	v_lshl_add_u64 v[174:175], v[144:145], 0, s[20:21]
	s_mov_b64 s[20:21], 0x40000
	v_lshl_add_u64 v[176:177], v[144:145], 0, s[20:21]
	s_mov_b64 s[20:21], 0x48000
	v_lshl_add_u64 v[178:179], v[144:145], 0, s[20:21]
	s_mov_b64 s[20:21], 0x50000
	v_lshl_add_u64 v[204:205], v[144:145], 0, s[20:21]
	s_mov_b64 s[20:21], 0x58000
	v_lshl_add_u64 v[206:207], v[144:145], 0, s[20:21]
	global_load_dwordx4 v[132:135], v[146:147], off
	global_load_dwordx4 v[208:211], v[146:147], off offset:64
	global_load_dwordx4 v[212:215], v[146:147], off offset:512
	global_load_dwordx4 v[216:219], v[146:147], off offset:576
	global_load_dwordx2 v[180:181], v[144:145], off
	global_load_dwordx2 v[182:183], v[168:169], off
	global_load_dwordx2 v[184:185], v[172:173], off
	global_load_dwordx2 v[186:187], v[174:175], off
	global_load_dwordx2 v[188:189], v[176:177], off
	global_load_dwordx2 v[190:191], v[178:179], off
	global_load_dwordx2 v[192:193], v[204:205], off
	global_load_dwordx2 v[194:195], v[206:207], off
	global_load_dwordx2 v[196:197], v[144:145], off offset:32
	global_load_dwordx2 v[198:199], v[168:169], off offset:32
	global_load_dwordx2 v[200:201], v[172:173], off offset:32
	global_load_dwordx2 v[202:203], v[174:175], off offset:32
	s_and_b64 vcc, exec, s[16:17]
	s_mov_b32 s47, s46
	s_mov_b64 s[24:25], s[12:13]
	s_mov_b64 s[22:23], s[14:15]
	s_mov_b32 s18, s45
	s_waitcnt vmcnt(11)
	v_lshlrev_b32_e32 v170, 16, v180
	v_and_b32_e32 v171, 0xffff0000, v180
	v_lshlrev_b32_e32 v180, 16, v181
	v_and_b32_e32 v181, 0xffff0000, v181
	v_pk_fma_f32 v[128:129], v[128:129], v[132:133], v[170:171]
	v_pk_fma_f32 v[130:131], v[130:131], v[134:135], v[180:181]
	v_cvt_pk_bf16_f32 v128, v128, v129
	s_nop 0
	v_cvt_pk_bf16_f32 v129, v130, v131
	global_store_dwordx2 v[144:145], v[128:129], off
	global_load_dwordx2 v[180:181], v[176:177], off offset:32
	s_waitcnt vmcnt(12)
	v_lshlrev_b32_e32 v170, 16, v182
	v_and_b32_e32 v171, 0xffff0000, v182
	v_lshlrev_b32_e32 v182, 16, v183
	v_and_b32_e32 v183, 0xffff0000, v183
	v_pk_fma_f32 v[124:125], v[124:125], v[132:133], v[170:171]
	v_pk_fma_f32 v[126:127], v[126:127], v[134:135], v[182:183]
	v_cvt_pk_bf16_f32 v124, v124, v125
	s_nop 0
	v_cvt_pk_bf16_f32 v125, v126, v127
	global_store_dwordx2 v[168:169], v[124:125], off
	global_load_dwordx2 v[182:183], v[178:179], off offset:32
	s_waitcnt vmcnt(13)
	v_lshlrev_b32_e32 v170, 16, v184
	v_and_b32_e32 v171, 0xffff0000, v184
	v_lshlrev_b32_e32 v184, 16, v185
	v_and_b32_e32 v185, 0xffff0000, v185
	v_pk_fma_f32 v[120:121], v[120:121], v[132:133], v[170:171]
	v_pk_fma_f32 v[122:123], v[122:123], v[134:135], v[184:185]
	v_cvt_pk_bf16_f32 v120, v120, v121
	s_nop 0
	v_cvt_pk_bf16_f32 v121, v122, v123
	global_store_dwordx2 v[172:173], v[120:121], off
	global_load_dwordx2 v[184:185], v[204:205], off offset:32
	s_waitcnt vmcnt(14)
	v_lshlrev_b32_e32 v170, 16, v186
	v_and_b32_e32 v171, 0xffff0000, v186
	v_lshlrev_b32_e32 v186, 16, v187
	v_and_b32_e32 v187, 0xffff0000, v187
	v_pk_fma_f32 v[116:117], v[116:117], v[132:133], v[170:171]
	v_pk_fma_f32 v[118:119], v[118:119], v[134:135], v[186:187]
	v_cvt_pk_bf16_f32 v116, v116, v117
	s_nop 0
	v_cvt_pk_bf16_f32 v117, v118, v119
	global_store_dwordx2 v[174:175], v[116:117], off
	global_load_dwordx2 v[186:187], v[206:207], off offset:32
	s_waitcnt vmcnt(15)
	v_lshlrev_b32_e32 v170, 16, v188
	v_and_b32_e32 v171, 0xffff0000, v188
	v_lshlrev_b32_e32 v188, 16, v189
	v_and_b32_e32 v189, 0xffff0000, v189
	v_pk_fma_f32 v[112:113], v[112:113], v[132:133], v[170:171]
	v_pk_fma_f32 v[114:115], v[114:115], v[134:135], v[188:189]
	v_cvt_pk_bf16_f32 v112, v112, v113
	s_nop 0
	v_cvt_pk_bf16_f32 v113, v114, v115
	global_store_dwordx2 v[176:177], v[112:113], off
	global_load_dwordx2 v[188:189], v[144:145], off offset:256
	s_waitcnt vmcnt(16)
	v_lshlrev_b32_e32 v170, 16, v190
	v_and_b32_e32 v171, 0xffff0000, v190
	v_lshlrev_b32_e32 v190, 16, v191
	v_and_b32_e32 v191, 0xffff0000, v191
	v_pk_fma_f32 v[108:109], v[108:109], v[132:133], v[170:171]
	v_pk_fma_f32 v[110:111], v[110:111], v[134:135], v[190:191]
	v_cvt_pk_bf16_f32 v108, v108, v109
	s_nop 0
	v_cvt_pk_bf16_f32 v109, v110, v111
	global_store_dwordx2 v[178:179], v[108:109], off
	global_load_dwordx2 v[190:191], v[168:169], off offset:256
	s_waitcnt vmcnt(17)
	v_lshlrev_b32_e32 v170, 16, v192
	v_and_b32_e32 v171, 0xffff0000, v192
	v_lshlrev_b32_e32 v192, 16, v193
	v_and_b32_e32 v193, 0xffff0000, v193
	v_pk_fma_f32 v[104:105], v[104:105], v[132:133], v[170:171]
	v_pk_fma_f32 v[106:107], v[106:107], v[134:135], v[192:193]
	v_cvt_pk_bf16_f32 v104, v104, v105
	s_nop 0
	v_cvt_pk_bf16_f32 v105, v106, v107
	global_store_dwordx2 v[204:205], v[104:105], off
	global_load_dwordx2 v[192:193], v[172:173], off offset:256
	s_waitcnt vmcnt(18)
	v_lshlrev_b32_e32 v170, 16, v194
	v_and_b32_e32 v171, 0xffff0000, v194
	v_lshlrev_b32_e32 v194, 16, v195
	v_and_b32_e32 v195, 0xffff0000, v195
	v_pk_fma_f32 v[92:93], v[92:93], v[132:133], v[170:171]
	v_pk_fma_f32 v[94:95], v[94:95], v[134:135], v[194:195]
	v_cvt_pk_bf16_f32 v92, v92, v93
	s_nop 0
	v_cvt_pk_bf16_f32 v93, v94, v95
	global_store_dwordx2 v[206:207], v[92:93], off
	global_load_dwordx2 v[194:195], v[174:175], off offset:256
	s_waitcnt vmcnt(19)
	v_lshlrev_b32_e32 v170, 16, v196
	v_and_b32_e32 v171, 0xffff0000, v196
	v_lshlrev_b32_e32 v196, 16, v197
	v_and_b32_e32 v197, 0xffff0000, v197
	v_pk_fma_f32 v[100:101], v[100:101], v[208:209], v[170:171]
	v_pk_fma_f32 v[102:103], v[102:103], v[210:211], v[196:197]
	v_cvt_pk_bf16_f32 v100, v100, v101
	s_nop 0
	v_cvt_pk_bf16_f32 v101, v102, v103
	global_store_dwordx2 v[144:145], v[100:101], off offset:32
	global_load_dwordx2 v[196:197], v[176:177], off offset:256
	s_waitcnt vmcnt(20)
	v_lshlrev_b32_e32 v170, 16, v198
	v_and_b32_e32 v171, 0xffff0000, v198
	v_lshlrev_b32_e32 v198, 16, v199
	v_and_b32_e32 v199, 0xffff0000, v199
	v_pk_fma_f32 v[96:97], v[96:97], v[208:209], v[170:171]
	v_pk_fma_f32 v[98:99], v[98:99], v[210:211], v[198:199]
	v_cvt_pk_bf16_f32 v96, v96, v97
	s_nop 0
	v_cvt_pk_bf16_f32 v97, v98, v99
	global_store_dwordx2 v[168:169], v[96:97], off offset:32
	global_load_dwordx2 v[198:199], v[178:179], off offset:256
	s_waitcnt vmcnt(21)
	v_lshlrev_b32_e32 v170, 16, v200
	v_and_b32_e32 v171, 0xffff0000, v200
	v_lshlrev_b32_e32 v200, 16, v201
	v_and_b32_e32 v201, 0xffff0000, v201
	v_pk_fma_f32 v[88:89], v[88:89], v[208:209], v[170:171]
	v_pk_fma_f32 v[90:91], v[90:91], v[210:211], v[200:201]
	v_cvt_pk_bf16_f32 v88, v88, v89
	s_nop 0
	v_cvt_pk_bf16_f32 v89, v90, v91
	global_store_dwordx2 v[172:173], v[88:89], off offset:32
	global_load_dwordx2 v[200:201], v[204:205], off offset:256
	s_waitcnt vmcnt(22)
	v_lshlrev_b32_e32 v170, 16, v202
	v_and_b32_e32 v171, 0xffff0000, v202
	v_lshlrev_b32_e32 v202, 16, v203
	v_and_b32_e32 v203, 0xffff0000, v203
	v_pk_fma_f32 v[84:85], v[84:85], v[208:209], v[170:171]
	v_pk_fma_f32 v[86:87], v[86:87], v[210:211], v[202:203]
	v_cvt_pk_bf16_f32 v84, v84, v85
	s_nop 0
	v_cvt_pk_bf16_f32 v85, v86, v87
	global_store_dwordx2 v[174:175], v[84:85], off offset:32
	global_load_dwordx2 v[202:203], v[206:207], off offset:256
	s_waitcnt vmcnt(22)
	v_lshlrev_b32_e32 v170, 16, v180
	v_and_b32_e32 v171, 0xffff0000, v180
	v_lshlrev_b32_e32 v180, 16, v181
	v_and_b32_e32 v181, 0xffff0000, v181
	v_pk_fma_f32 v[78:79], v[78:79], v[208:209], v[170:171]
	v_pk_fma_f32 v[80:81], v[80:81], v[210:211], v[180:181]
	v_cvt_pk_bf16_f32 v78, v78, v79
	s_nop 0
	v_cvt_pk_bf16_f32 v79, v80, v81
	global_store_dwordx2 v[176:177], v[78:79], off offset:32
	global_load_dwordx2 v[180:181], v[144:145], off offset:288
	s_waitcnt vmcnt(22)
	v_lshlrev_b32_e32 v170, 16, v182
	v_and_b32_e32 v171, 0xffff0000, v182
	v_lshlrev_b32_e32 v182, 16, v183
	v_and_b32_e32 v183, 0xffff0000, v183
	v_pk_fma_f32 v[74:75], v[74:75], v[208:209], v[170:171]
	v_pk_fma_f32 v[76:77], v[76:77], v[210:211], v[182:183]
	v_cvt_pk_bf16_f32 v74, v74, v75
	s_nop 0
	v_cvt_pk_bf16_f32 v75, v76, v77
	global_store_dwordx2 v[178:179], v[74:75], off offset:32
	global_load_dwordx2 v[182:183], v[168:169], off offset:288
	s_waitcnt vmcnt(22)
	v_lshlrev_b32_e32 v170, 16, v184
	v_and_b32_e32 v171, 0xffff0000, v184
	v_lshlrev_b32_e32 v184, 16, v185
	v_and_b32_e32 v185, 0xffff0000, v185
	v_pk_fma_f32 v[70:71], v[70:71], v[208:209], v[170:171]
	v_pk_fma_f32 v[72:73], v[72:73], v[210:211], v[184:185]
	v_cvt_pk_bf16_f32 v70, v70, v71
	s_nop 0
	v_cvt_pk_bf16_f32 v71, v72, v73
	global_store_dwordx2 v[204:205], v[70:71], off offset:32
	global_load_dwordx2 v[184:185], v[172:173], off offset:288
	s_waitcnt vmcnt(22)
	v_lshlrev_b32_e32 v170, 16, v186
	v_and_b32_e32 v171, 0xffff0000, v186
	v_lshlrev_b32_e32 v186, 16, v187
	v_and_b32_e32 v187, 0xffff0000, v187
	v_pk_fma_f32 v[62:63], v[62:63], v[208:209], v[170:171]
	v_pk_fma_f32 v[64:65], v[64:65], v[210:211], v[186:187]
	v_cvt_pk_bf16_f32 v62, v62, v63
	s_nop 0
	v_cvt_pk_bf16_f32 v63, v64, v65
	global_store_dwordx2 v[206:207], v[62:63], off offset:32
	global_load_dwordx2 v[186:187], v[174:175], off offset:288
	s_waitcnt vmcnt(22)
	v_lshlrev_b32_e32 v170, 16, v188
	v_and_b32_e32 v171, 0xffff0000, v188
	v_lshlrev_b32_e32 v188, 16, v189
	v_and_b32_e32 v189, 0xffff0000, v189
	v_pk_fma_f32 v[66:67], v[66:67], v[212:213], v[170:171]
	v_pk_fma_f32 v[68:69], v[68:69], v[214:215], v[188:189]
	v_cvt_pk_bf16_f32 v66, v66, v67
	s_nop 0
	v_cvt_pk_bf16_f32 v67, v68, v69
	global_store_dwordx2 v[144:145], v[66:67], off offset:256
	global_load_dwordx2 v[188:189], v[176:177], off offset:288
	s_waitcnt vmcnt(22)
	v_lshlrev_b32_e32 v170, 16, v190
	v_and_b32_e32 v171, 0xffff0000, v190
	v_lshlrev_b32_e32 v190, 16, v191
	v_and_b32_e32 v191, 0xffff0000, v191
	v_pk_fma_f32 v[58:59], v[58:59], v[212:213], v[170:171]
	v_pk_fma_f32 v[60:61], v[60:61], v[214:215], v[190:191]
	v_cvt_pk_bf16_f32 v58, v58, v59
	s_nop 0
	v_cvt_pk_bf16_f32 v59, v60, v61
	global_store_dwordx2 v[168:169], v[58:59], off offset:256
	global_load_dwordx2 v[190:191], v[178:179], off offset:288
	s_waitcnt vmcnt(22)
	v_lshlrev_b32_e32 v170, 16, v192
	v_and_b32_e32 v171, 0xffff0000, v192
	v_lshlrev_b32_e32 v192, 16, v193
	v_and_b32_e32 v193, 0xffff0000, v193
	v_pk_fma_f32 v[54:55], v[54:55], v[212:213], v[170:171]
	v_pk_fma_f32 v[56:57], v[56:57], v[214:215], v[192:193]
	v_cvt_pk_bf16_f32 v54, v54, v55
	s_nop 0
	v_cvt_pk_bf16_f32 v55, v56, v57
	global_store_dwordx2 v[172:173], v[54:55], off offset:256
	global_load_dwordx2 v[192:193], v[204:205], off offset:288
	s_waitcnt vmcnt(22)
	v_lshlrev_b32_e32 v170, 16, v194
	v_and_b32_e32 v171, 0xffff0000, v194
	v_lshlrev_b32_e32 v194, 16, v195
	v_and_b32_e32 v195, 0xffff0000, v195
	v_pk_fma_f32 v[50:51], v[50:51], v[212:213], v[170:171]
	v_pk_fma_f32 v[52:53], v[52:53], v[214:215], v[194:195]
	v_cvt_pk_bf16_f32 v50, v50, v51
	s_nop 0
	v_cvt_pk_bf16_f32 v51, v52, v53
	global_store_dwordx2 v[174:175], v[50:51], off offset:256
	global_load_dwordx2 v[194:195], v[206:207], off offset:288
	s_waitcnt vmcnt(22)
	v_lshlrev_b32_e32 v170, 16, v196
	v_and_b32_e32 v171, 0xffff0000, v196
	v_lshlrev_b32_e32 v196, 16, v197
	v_and_b32_e32 v197, 0xffff0000, v197
	v_pk_fma_f32 v[46:47], v[46:47], v[212:213], v[170:171]
	v_pk_fma_f32 v[48:49], v[48:49], v[214:215], v[196:197]
	v_cvt_pk_bf16_f32 v46, v46, v47
	s_nop 0
	v_cvt_pk_bf16_f32 v47, v48, v49
	global_store_dwordx2 v[176:177], v[46:47], off offset:256
	s_waitcnt vmcnt(21)
	v_lshlrev_b32_e32 v170, 16, v198
	v_and_b32_e32 v171, 0xffff0000, v198
	v_lshlrev_b32_e32 v198, 16, v199
	v_and_b32_e32 v199, 0xffff0000, v199
	v_pk_fma_f32 v[42:43], v[42:43], v[212:213], v[170:171]
	v_pk_fma_f32 v[44:45], v[44:45], v[214:215], v[198:199]
	v_cvt_pk_bf16_f32 v42, v42, v43
	s_nop 0
	v_cvt_pk_bf16_f32 v43, v44, v45
	global_store_dwordx2 v[178:179], v[42:43], off offset:256
	s_waitcnt vmcnt(20)
	v_lshlrev_b32_e32 v170, 16, v200
	v_and_b32_e32 v171, 0xffff0000, v200
	v_lshlrev_b32_e32 v200, 16, v201
	v_and_b32_e32 v201, 0xffff0000, v201
	v_pk_fma_f32 v[34:35], v[34:35], v[212:213], v[170:171]
	v_pk_fma_f32 v[36:37], v[36:37], v[214:215], v[200:201]
	v_cvt_pk_bf16_f32 v34, v34, v35
	s_nop 0
	v_cvt_pk_bf16_f32 v35, v36, v37
	global_store_dwordx2 v[204:205], v[34:35], off offset:256
	s_waitcnt vmcnt(19)
	v_lshlrev_b32_e32 v170, 16, v202
	v_and_b32_e32 v171, 0xffff0000, v202
	v_lshlrev_b32_e32 v202, 16, v203
	v_and_b32_e32 v203, 0xffff0000, v203
	v_pk_fma_f32 v[26:27], v[26:27], v[212:213], v[170:171]
	v_pk_fma_f32 v[28:29], v[28:29], v[214:215], v[202:203]
	v_cvt_pk_bf16_f32 v26, v26, v27
	s_nop 0
	v_cvt_pk_bf16_f32 v27, v28, v29
	global_store_dwordx2 v[206:207], v[26:27], off offset:256
	s_waitcnt vmcnt(18)
	v_lshlrev_b32_e32 v170, 16, v180
	v_and_b32_e32 v171, 0xffff0000, v180
	v_lshlrev_b32_e32 v180, 16, v181
	v_and_b32_e32 v181, 0xffff0000, v181
	v_pk_fma_f32 v[38:39], v[38:39], v[216:217], v[170:171]
	v_pk_fma_f32 v[40:41], v[40:41], v[218:219], v[180:181]
	v_cvt_pk_bf16_f32 v38, v38, v39
	s_nop 0
	v_cvt_pk_bf16_f32 v39, v40, v41
	global_store_dwordx2 v[144:145], v[38:39], off offset:288
	s_waitcnt vmcnt(17)
	v_lshlrev_b32_e32 v170, 16, v182
	v_and_b32_e32 v171, 0xffff0000, v182
	v_lshlrev_b32_e32 v182, 16, v183
	v_and_b32_e32 v183, 0xffff0000, v183
	v_pk_fma_f32 v[30:31], v[30:31], v[216:217], v[170:171]
	v_pk_fma_f32 v[32:33], v[32:33], v[218:219], v[182:183]
	v_cvt_pk_bf16_f32 v30, v30, v31
	s_nop 0
	v_cvt_pk_bf16_f32 v31, v32, v33
	global_store_dwordx2 v[168:169], v[30:31], off offset:288
	s_waitcnt vmcnt(16)
	v_lshlrev_b32_e32 v170, 16, v184
	v_and_b32_e32 v171, 0xffff0000, v184
	v_lshlrev_b32_e32 v184, 16, v185
	v_and_b32_e32 v185, 0xffff0000, v185
	v_pk_fma_f32 v[22:23], v[22:23], v[216:217], v[170:171]
	v_pk_fma_f32 v[24:25], v[24:25], v[218:219], v[184:185]
	v_cvt_pk_bf16_f32 v22, v22, v23
	s_nop 0
	v_cvt_pk_bf16_f32 v23, v24, v25
	global_store_dwordx2 v[172:173], v[22:23], off offset:288
	s_waitcnt vmcnt(15)
	v_lshlrev_b32_e32 v170, 16, v186
	v_and_b32_e32 v171, 0xffff0000, v186
	v_lshlrev_b32_e32 v186, 16, v187
	v_and_b32_e32 v187, 0xffff0000, v187
	v_pk_fma_f32 v[18:19], v[18:19], v[216:217], v[170:171]
	v_pk_fma_f32 v[20:21], v[20:21], v[218:219], v[186:187]
	v_cvt_pk_bf16_f32 v18, v18, v19
	s_nop 0
	v_cvt_pk_bf16_f32 v19, v20, v21
	global_store_dwordx2 v[174:175], v[18:19], off offset:288
	s_waitcnt vmcnt(14)
	v_lshlrev_b32_e32 v170, 16, v188
	v_and_b32_e32 v171, 0xffff0000, v188
	v_lshlrev_b32_e32 v188, 16, v189
	v_and_b32_e32 v189, 0xffff0000, v189
	v_pk_fma_f32 v[14:15], v[14:15], v[216:217], v[170:171]
	v_pk_fma_f32 v[16:17], v[16:17], v[218:219], v[188:189]
	v_cvt_pk_bf16_f32 v14, v14, v15
	s_nop 0
	v_cvt_pk_bf16_f32 v15, v16, v17
	global_store_dwordx2 v[176:177], v[14:15], off offset:288
	s_waitcnt vmcnt(13)
	v_lshlrev_b32_e32 v170, 16, v190
	v_and_b32_e32 v171, 0xffff0000, v190
	v_lshlrev_b32_e32 v190, 16, v191
	v_and_b32_e32 v191, 0xffff0000, v191
	v_pk_fma_f32 v[10:11], v[10:11], v[216:217], v[170:171]
	v_pk_fma_f32 v[12:13], v[12:13], v[218:219], v[190:191]
	v_cvt_pk_bf16_f32 v10, v10, v11
	s_nop 0
	v_cvt_pk_bf16_f32 v11, v12, v13
	global_store_dwordx2 v[178:179], v[10:11], off offset:288
	s_waitcnt vmcnt(12)
	v_lshlrev_b32_e32 v170, 16, v192
	v_and_b32_e32 v171, 0xffff0000, v192
	v_lshlrev_b32_e32 v192, 16, v193
	v_and_b32_e32 v193, 0xffff0000, v193
	v_pk_fma_f32 v[6:7], v[6:7], v[216:217], v[170:171]
	v_pk_fma_f32 v[8:9], v[8:9], v[218:219], v[192:193]
	v_cvt_pk_bf16_f32 v6, v6, v7
	s_nop 0
	v_cvt_pk_bf16_f32 v7, v8, v9
	global_store_dwordx2 v[204:205], v[6:7], off offset:288
	s_waitcnt vmcnt(11)
	v_lshlrev_b32_e32 v170, 16, v194
	v_and_b32_e32 v171, 0xffff0000, v194
	v_lshlrev_b32_e32 v194, 16, v195
	v_and_b32_e32 v195, 0xffff0000, v195
	v_pk_fma_f32 v[2:3], v[2:3], v[216:217], v[170:171]
	v_pk_fma_f32 v[4:5], v[4:5], v[218:219], v[194:195]
	v_cvt_pk_bf16_f32 v2, v2, v3
	s_nop 0
	v_cvt_pk_bf16_f32 v3, v4, v5
	global_store_dwordx2 v[206:207], v[2:3], off offset:288
	s_cbranch_vccz .LBB0_1539
	s_waitcnt vmcnt(0)
	s_cmpk_gt_u32 s41, 0xff
	s_cbranch_scc1 .LBB0_1546
	s_barrier

.LBB0_1632:
	v_lshl_add_u64 v[28:29], v[110:111], 0, s[0:1]
	v_add_co_u32_e32 v32, vcc, 0xe5f0000, v28
	s_add_u32 s0, s0, 0x200
	s_nop 0
	v_addc_co_u32_e32 v33, vcc, 0, v29, vcc
	global_load_dwordx4 v[38:41], v[32:33], off
	global_load_dwordx4 v[42:45], v[32:33], off offset:64
	global_load_dwordx4 v[46:49], v[32:33], off offset:128
	global_load_dwordx4 v[50:53], v[32:33], off offset:192
	global_load_dwordx4 v[54:57], v[32:33], off offset:256
	global_load_dwordx4 v[58:61], v[32:33], off offset:320
	global_load_dwordx4 v[62:65], v[32:33], off offset:384
	global_load_dwordx4 v[66:69], v[32:33], off offset:448
	s_addc_u32 s1, s1, 0
	s_cmpk_lg_i32 s0, 0x800
	s_waitcnt vmcnt(7)
	v_lshlrev_b32_e32 v34, 16, v38
	v_and_b32_e32 v35, 0xffff0000, v38
	v_pk_mul_f32 v[34:35], v[34:35], v[34:35]
	v_and_b32_e32 v28, 0xffff0000, v39
	v_lshlrev_b32_e32 v29, 16, v39
	v_pk_mul_f32 v[28:29], v[28:29], v[28:29]
	v_add_f32_e32 v27, v34, v35
	v_and_b32_e32 v36, 0xffff0000, v40
	v_lshlrev_b32_e32 v37, 16, v40
	v_add_f32_e32 v27, v29, v27
	v_pk_mul_f32 v[36:37], v[36:37], v[36:37]
	v_add_f32_e32 v27, v28, v27
	v_and_b32_e32 v30, 0xffff0000, v41
	v_lshlrev_b32_e32 v31, 16, v41
	v_add_f32_e32 v27, v37, v27
	v_pk_mul_f32 v[30:31], v[30:31], v[30:31]
	v_add_f32_e32 v27, v36, v27
	v_add_f32_e32 v27, v31, v27
	v_add_f32_e32 v27, v30, v27
	v_add_f32_e32 v23, v23, v27
	s_waitcnt vmcnt(6)
	v_lshlrev_b32_e32 v34, 16, v42
	v_and_b32_e32 v35, 0xffff0000, v42
	v_pk_mul_f32 v[34:35], v[34:35], v[34:35]
	v_and_b32_e32 v28, 0xffff0000, v43
	v_lshlrev_b32_e32 v29, 16, v43
	v_pk_mul_f32 v[28:29], v[28:29], v[28:29]
	v_add_f32_e32 v27, v34, v35
	v_and_b32_e32 v36, 0xffff0000, v44
	v_lshlrev_b32_e32 v37, 16, v44
	v_add_f32_e32 v27, v29, v27
	v_pk_mul_f32 v[36:37], v[36:37], v[36:37]
	v_add_f32_e32 v27, v28, v27
	v_and_b32_e32 v30, 0xffff0000, v45
	v_lshlrev_b32_e32 v31, 16, v45
	v_add_f32_e32 v27, v37, v27
	v_pk_mul_f32 v[30:31], v[30:31], v[30:31]
	v_add_f32_e32 v27, v36, v27
	v_add_f32_e32 v27, v31, v27
	v_add_f32_e32 v27, v30, v27
	v_add_f32_e32 v23, v23, v27
	s_waitcnt vmcnt(5)
	v_lshlrev_b32_e32 v34, 16, v46
	v_and_b32_e32 v35, 0xffff0000, v46
	v_pk_mul_f32 v[34:35], v[34:35], v[34:35]
	v_and_b32_e32 v28, 0xffff0000, v47
	v_lshlrev_b32_e32 v29, 16, v47
	v_pk_mul_f32 v[28:29], v[28:29], v[28:29]
	v_add_f32_e32 v27, v34, v35
	v_and_b32_e32 v36, 0xffff0000, v48
	v_lshlrev_b32_e32 v37, 16, v48
	v_add_f32_e32 v27, v29, v27
	v_pk_mul_f32 v[36:37], v[36:37], v[36:37]
	v_add_f32_e32 v27, v28, v27
	v_and_b32_e32 v30, 0xffff0000, v49
	v_lshlrev_b32_e32 v31, 16, v49
	v_add_f32_e32 v27, v37, v27
	v_pk_mul_f32 v[30:31], v[30:31], v[30:31]
	v_add_f32_e32 v27, v36, v27
	v_add_f32_e32 v27, v31, v27
	v_add_f32_e32 v27, v30, v27
	v_add_f32_e32 v23, v23, v27
	s_waitcnt vmcnt(4)
	v_lshlrev_b32_e32 v34, 16, v50
	v_and_b32_e32 v35, 0xffff0000, v50
	v_pk_mul_f32 v[34:35], v[34:35], v[34:35]
	v_and_b32_e32 v28, 0xffff0000, v51
	v_lshlrev_b32_e32 v29, 16, v51
	v_pk_mul_f32 v[28:29], v[28:29], v[28:29]
	v_add_f32_e32 v27, v34, v35
	v_and_b32_e32 v36, 0xffff0000, v52
	v_lshlrev_b32_e32 v37, 16, v52
	v_add_f32_e32 v27, v29, v27
	v_pk_mul_f32 v[36:37], v[36:37], v[36:37]
	v_add_f32_e32 v27, v28, v27
	v_and_b32_e32 v30, 0xffff0000, v53
	v_lshlrev_b32_e32 v31, 16, v53
	v_add_f32_e32 v27, v37, v27
	v_pk_mul_f32 v[30:31], v[30:31], v[30:31]
	v_add_f32_e32 v27, v36, v27
	v_add_f32_e32 v27, v31, v27
	v_add_f32_e32 v27, v30, v27
	v_add_f32_e32 v23, v23, v27
	s_waitcnt vmcnt(3)
	v_lshlrev_b32_e32 v34, 16, v54
	v_and_b32_e32 v35, 0xffff0000, v54
	v_pk_mul_f32 v[34:35], v[34:35], v[34:35]
	v_and_b32_e32 v28, 0xffff0000, v55
	v_lshlrev_b32_e32 v29, 16, v55
	v_pk_mul_f32 v[28:29], v[28:29], v[28:29]
	v_add_f32_e32 v27, v34, v35
	v_and_b32_e32 v36, 0xffff0000, v56
	v_lshlrev_b32_e32 v37, 16, v56
	v_add_f32_e32 v27, v29, v27
	v_pk_mul_f32 v[36:37], v[36:37], v[36:37]
	v_add_f32_e32 v27, v28, v27
	v_and_b32_e32 v30, 0xffff0000, v57
	v_lshlrev_b32_e32 v31, 16, v57
	v_add_f32_e32 v27, v37, v27
	v_pk_mul_f32 v[30:31], v[30:31], v[30:31]
	v_add_f32_e32 v27, v36, v27
	v_add_f32_e32 v27, v31, v27
	v_add_f32_e32 v27, v30, v27
	v_add_f32_e32 v23, v23, v27
	s_waitcnt vmcnt(2)
	v_lshlrev_b32_e32 v34, 16, v58
	v_and_b32_e32 v35, 0xffff0000, v58
	v_pk_mul_f32 v[34:35], v[34:35], v[34:35]
	v_and_b32_e32 v28, 0xffff0000, v59
	v_lshlrev_b32_e32 v29, 16, v59
	v_pk_mul_f32 v[28:29], v[28:29], v[28:29]
	v_add_f32_e32 v27, v34, v35
	v_and_b32_e32 v36, 0xffff0000, v60
	v_lshlrev_b32_e32 v37, 16, v60
	v_add_f32_e32 v27, v29, v27
	v_pk_mul_f32 v[36:37], v[36:37], v[36:37]
	v_add_f32_e32 v27, v28, v27
	v_and_b32_e32 v30, 0xffff0000, v61
	v_lshlrev_b32_e32 v31, 16, v61
	v_add_f32_e32 v27, v37, v27
	v_pk_mul_f32 v[30:31], v[30:31], v[30:31]
	v_add_f32_e32 v27, v36, v27
	v_add_f32_e32 v27, v31, v27
	v_add_f32_e32 v27, v30, v27
	v_add_f32_e32 v23, v23, v27
	s_waitcnt vmcnt(1)
	v_lshlrev_b32_e32 v34, 16, v62
	v_and_b32_e32 v35, 0xffff0000, v62
	v_pk_mul_f32 v[34:35], v[34:35], v[34:35]
	v_and_b32_e32 v28, 0xffff0000, v63
	v_lshlrev_b32_e32 v29, 16, v63
	v_pk_mul_f32 v[28:29], v[28:29], v[28:29]
	v_add_f32_e32 v27, v34, v35
	v_and_b32_e32 v36, 0xffff0000, v64
	v_lshlrev_b32_e32 v37, 16, v64
	v_add_f32_e32 v27, v29, v27
	v_pk_mul_f32 v[36:37], v[36:37], v[36:37]
	v_add_f32_e32 v27, v28, v27
	v_and_b32_e32 v30, 0xffff0000, v65
	v_lshlrev_b32_e32 v31, 16, v65
	v_add_f32_e32 v27, v37, v27
	v_pk_mul_f32 v[30:31], v[30:31], v[30:31]
	v_add_f32_e32 v27, v36, v27
	v_add_f32_e32 v27, v31, v27
	v_add_f32_e32 v27, v30, v27
	v_add_f32_e32 v23, v23, v27
	s_waitcnt vmcnt(0)
	v_lshlrev_b32_e32 v34, 16, v66
	v_and_b32_e32 v35, 0xffff0000, v66
	v_pk_mul_f32 v[34:35], v[34:35], v[34:35]
	v_and_b32_e32 v28, 0xffff0000, v67
	v_lshlrev_b32_e32 v29, 16, v67
	v_pk_mul_f32 v[28:29], v[28:29], v[28:29]
	v_add_f32_e32 v27, v34, v35
	v_and_b32_e32 v36, 0xffff0000, v68
	v_lshlrev_b32_e32 v37, 16, v68
	v_add_f32_e32 v27, v29, v27
	v_pk_mul_f32 v[36:37], v[36:37], v[36:37]
	v_add_f32_e32 v27, v28, v27
	v_and_b32_e32 v30, 0xffff0000, v69
	v_lshlrev_b32_e32 v31, 16, v69
	v_add_f32_e32 v27, v37, v27
	v_pk_mul_f32 v[30:31], v[30:31], v[30:31]
	v_add_f32_e32 v27, v36, v27
	v_add_f32_e32 v27, v31, v27
	v_add_f32_e32 v27, v30, v27
	v_add_f32_e32 v23, v23, v27
	s_cbranch_scc1 .LBB0_1632
	v_lshl_add_u64 v[112:113], v[92:93], 0, v[24:25]
	ds_swizzle_b32 v24, v23 offset:swizzle(SWAP,16)
	s_add_i32 s42, s40, 8
	s_cmp_lt_i32 s42, s41
	v_min_i32_e32 v26, 0x8000, v26
	s_cselect_b64 s[0:1], -1, 0
	s_waitcnt lgkmcnt(0)
	v_add_f32_e32 v23, v23, v24
	v_mov_b32_e32 v24, v23
	s_nop 1
	v_permlane32_swap_b32_e32 v23, v24
	v_add_f32_e32 v23, v23, v24
	v_fmamk_f32 v23, v23, 0x3a800000, v224
	v_cmp_gt_f32_e32 vcc, s64, v23
	v_mul_f32_e32 v24, 0x4b800000, v23
	v_ashrrev_i32_e32 v26, 14, v26
	v_cndmask_b32_e32 v23, v23, v24, vcc
	v_rsq_f32_e32 v23, v23
	s_and_b64 s[34:35], s[6:7], s[0:1]
	s_movk_i32 s0, 0x3000
	v_mad_i32_i24 v131, v26, s0, v127
	v_mul_f32_e32 v24, 0x45800000, v23
	v_cndmask_b32_e32 v132, v23, v24, vcc
	v_add_u32_e32 v109, 0x1000, v131
	v_mov_b32_e32 v133, v131
	v_mov_b32_e32 v134, v132
	v_mov_b64_e32 v[114:115], v[112:113]
	s_and_saveexec_b64 s[0:1], s[34:35]
	s_cbranch_execnz .LBB0_1733
	s_or_b64 exec, exec, s[0:1]
	s_and_saveexec_b64 s[0:1], s[12:13]
	s_cbranch_execnz .LBB0_1736

.LBB0_1734:
	v_lshl_add_u64 v[26:27], v[22:23], 0, s[20:21]
	v_add_co_u32_e32 v30, vcc, 0xe5f0000, v26
	s_add_u32 s20, s20, 0x200
	s_nop 0
	v_addc_co_u32_e32 v31, vcc, 0, v27, vcc
	global_load_dwordx4 v[38:41], v[30:31], off
	global_load_dwordx4 v[42:45], v[30:31], off offset:64
	global_load_dwordx4 v[46:49], v[30:31], off offset:128
	global_load_dwordx4 v[50:53], v[30:31], off offset:192
	global_load_dwordx4 v[54:57], v[30:31], off offset:256
	global_load_dwordx4 v[58:61], v[30:31], off offset:320
	global_load_dwordx4 v[62:65], v[30:31], off offset:384
	global_load_dwordx4 v[66:69], v[30:31], off offset:448
	s_addc_u32 s21, s21, 0
	s_cmpk_lg_i32 s20, 0x800
	s_waitcnt vmcnt(7)
	v_lshlrev_b32_e32 v32, 16, v38
	v_and_b32_e32 v33, 0xffff0000, v38
	v_pk_mul_f32 v[32:33], v[32:33], v[32:33]
	v_and_b32_e32 v28, 0xffff0000, v39
	v_lshlrev_b32_e32 v29, 16, v39
	v_pk_mul_f32 v[28:29], v[28:29], v[28:29]
	v_add_f32_e32 v25, v32, v33
	v_and_b32_e32 v34, 0xffff0000, v40
	v_lshlrev_b32_e32 v35, 16, v40
	v_add_f32_e32 v25, v29, v25
	v_pk_mul_f32 v[34:35], v[34:35], v[34:35]
	v_add_f32_e32 v25, v28, v25
	v_and_b32_e32 v26, 0xffff0000, v41
	v_lshlrev_b32_e32 v27, 16, v41
	v_add_f32_e32 v25, v35, v25
	v_pk_mul_f32 v[26:27], v[26:27], v[26:27]
	v_add_f32_e32 v25, v34, v25
	v_add_f32_e32 v25, v27, v25
	v_add_f32_e32 v25, v26, v25
	v_add_f32_e32 v24, v24, v25
	s_waitcnt vmcnt(6)
	v_lshlrev_b32_e32 v32, 16, v42
	v_and_b32_e32 v33, 0xffff0000, v42
	v_pk_mul_f32 v[32:33], v[32:33], v[32:33]
	v_and_b32_e32 v28, 0xffff0000, v43
	v_lshlrev_b32_e32 v29, 16, v43
	v_pk_mul_f32 v[28:29], v[28:29], v[28:29]
	v_add_f32_e32 v25, v32, v33
	v_and_b32_e32 v34, 0xffff0000, v44
	v_lshlrev_b32_e32 v35, 16, v44
	v_add_f32_e32 v25, v29, v25
	v_pk_mul_f32 v[34:35], v[34:35], v[34:35]
	v_add_f32_e32 v25, v28, v25
	v_and_b32_e32 v26, 0xffff0000, v45
	v_lshlrev_b32_e32 v27, 16, v45
	v_add_f32_e32 v25, v35, v25
	v_pk_mul_f32 v[26:27], v[26:27], v[26:27]
	v_add_f32_e32 v25, v34, v25
	v_add_f32_e32 v25, v27, v25
	v_add_f32_e32 v25, v26, v25
	v_add_f32_e32 v24, v24, v25
	s_waitcnt vmcnt(5)
	v_lshlrev_b32_e32 v32, 16, v46
	v_and_b32_e32 v33, 0xffff0000, v46
	v_pk_mul_f32 v[32:33], v[32:33], v[32:33]
	v_and_b32_e32 v28, 0xffff0000, v47
	v_lshlrev_b32_e32 v29, 16, v47
	v_pk_mul_f32 v[28:29], v[28:29], v[28:29]
	v_add_f32_e32 v25, v32, v33
	v_and_b32_e32 v34, 0xffff0000, v48
	v_lshlrev_b32_e32 v35, 16, v48
	v_add_f32_e32 v25, v29, v25
	v_pk_mul_f32 v[34:35], v[34:35], v[34:35]
	v_add_f32_e32 v25, v28, v25
	v_and_b32_e32 v26, 0xffff0000, v49
	v_lshlrev_b32_e32 v27, 16, v49
	v_add_f32_e32 v25, v35, v25
	v_pk_mul_f32 v[26:27], v[26:27], v[26:27]
	v_add_f32_e32 v25, v34, v25
	v_add_f32_e32 v25, v27, v25
	v_add_f32_e32 v25, v26, v25
	v_add_f32_e32 v24, v24, v25
	s_waitcnt vmcnt(4)
	v_lshlrev_b32_e32 v32, 16, v50
	v_and_b32_e32 v33, 0xffff0000, v50
	v_pk_mul_f32 v[32:33], v[32:33], v[32:33]
	v_and_b32_e32 v28, 0xffff0000, v51
	v_lshlrev_b32_e32 v29, 16, v51
	v_pk_mul_f32 v[28:29], v[28:29], v[28:29]
	v_add_f32_e32 v25, v32, v33
	v_and_b32_e32 v34, 0xffff0000, v52
	v_lshlrev_b32_e32 v35, 16, v52
	v_add_f32_e32 v25, v29, v25
	v_pk_mul_f32 v[34:35], v[34:35], v[34:35]
	v_add_f32_e32 v25, v28, v25
	v_and_b32_e32 v26, 0xffff0000, v53
	v_lshlrev_b32_e32 v27, 16, v53
	v_add_f32_e32 v25, v35, v25
	v_pk_mul_f32 v[26:27], v[26:27], v[26:27]
	v_add_f32_e32 v25, v34, v25
	v_add_f32_e32 v25, v27, v25
	v_add_f32_e32 v25, v26, v25
	v_add_f32_e32 v24, v24, v25
	s_waitcnt vmcnt(3)
	v_lshlrev_b32_e32 v32, 16, v54
	v_and_b32_e32 v33, 0xffff0000, v54
	v_pk_mul_f32 v[32:33], v[32:33], v[32:33]
	v_and_b32_e32 v28, 0xffff0000, v55
	v_lshlrev_b32_e32 v29, 16, v55
	v_pk_mul_f32 v[28:29], v[28:29], v[28:29]
	v_add_f32_e32 v25, v32, v33
	v_and_b32_e32 v34, 0xffff0000, v56
	v_lshlrev_b32_e32 v35, 16, v56
	v_add_f32_e32 v25, v29, v25
	v_pk_mul_f32 v[34:35], v[34:35], v[34:35]
	v_add_f32_e32 v25, v28, v25
	v_and_b32_e32 v26, 0xffff0000, v57
	v_lshlrev_b32_e32 v27, 16, v57
	v_add_f32_e32 v25, v35, v25
	v_pk_mul_f32 v[26:27], v[26:27], v[26:27]
	v_add_f32_e32 v25, v34, v25
	v_add_f32_e32 v25, v27, v25
	v_add_f32_e32 v25, v26, v25
	v_add_f32_e32 v24, v24, v25
	s_waitcnt vmcnt(2)
	v_lshlrev_b32_e32 v32, 16, v58
	v_and_b32_e32 v33, 0xffff0000, v58
	v_pk_mul_f32 v[32:33], v[32:33], v[32:33]
	v_and_b32_e32 v28, 0xffff0000, v59
	v_lshlrev_b32_e32 v29, 16, v59
	v_pk_mul_f32 v[28:29], v[28:29], v[28:29]
	v_add_f32_e32 v25, v32, v33
	v_and_b32_e32 v34, 0xffff0000, v60
	v_lshlrev_b32_e32 v35, 16, v60
	v_add_f32_e32 v25, v29, v25
	v_pk_mul_f32 v[34:35], v[34:35], v[34:35]
	v_add_f32_e32 v25, v28, v25
	v_and_b32_e32 v26, 0xffff0000, v61
	v_lshlrev_b32_e32 v27, 16, v61
	v_add_f32_e32 v25, v35, v25
	v_pk_mul_f32 v[26:27], v[26:27], v[26:27]
	v_add_f32_e32 v25, v34, v25
	v_add_f32_e32 v25, v27, v25
	v_add_f32_e32 v25, v26, v25
	v_add_f32_e32 v24, v24, v25
	s_waitcnt vmcnt(1)
	v_lshlrev_b32_e32 v32, 16, v62
	v_and_b32_e32 v33, 0xffff0000, v62
	v_pk_mul_f32 v[32:33], v[32:33], v[32:33]
	v_and_b32_e32 v28, 0xffff0000, v63
	v_lshlrev_b32_e32 v29, 16, v63
	v_pk_mul_f32 v[28:29], v[28:29], v[28:29]
	v_add_f32_e32 v25, v32, v33
	v_and_b32_e32 v34, 0xffff0000, v64
	v_lshlrev_b32_e32 v35, 16, v64
	v_add_f32_e32 v25, v29, v25
	v_pk_mul_f32 v[34:35], v[34:35], v[34:35]
	v_add_f32_e32 v25, v28, v25
	v_and_b32_e32 v26, 0xffff0000, v65
	v_lshlrev_b32_e32 v27, 16, v65
	v_add_f32_e32 v25, v35, v25
	v_pk_mul_f32 v[26:27], v[26:27], v[26:27]
	v_add_f32_e32 v25, v34, v25
	v_add_f32_e32 v25, v27, v25
	v_add_f32_e32 v25, v26, v25
	v_add_f32_e32 v24, v24, v25
	s_waitcnt vmcnt(0)
	v_lshlrev_b32_e32 v32, 16, v66
	v_and_b32_e32 v33, 0xffff0000, v66
	v_pk_mul_f32 v[32:33], v[32:33], v[32:33]
	v_and_b32_e32 v28, 0xffff0000, v67
	v_lshlrev_b32_e32 v29, 16, v67
	v_pk_mul_f32 v[28:29], v[28:29], v[28:29]
	v_add_f32_e32 v25, v32, v33
	v_and_b32_e32 v34, 0xffff0000, v68
	v_lshlrev_b32_e32 v35, 16, v68
	v_add_f32_e32 v25, v29, v25
	v_pk_mul_f32 v[34:35], v[34:35], v[34:35]
	v_add_f32_e32 v25, v28, v25
	v_and_b32_e32 v26, 0xffff0000, v69
	v_lshlrev_b32_e32 v27, 16, v69
	v_add_f32_e32 v25, v35, v25
	v_pk_mul_f32 v[26:27], v[26:27], v[26:27]
	v_add_f32_e32 v25, v34, v25
	v_add_f32_e32 v25, v27, v25
	v_add_f32_e32 v25, v26, v25
	v_add_f32_e32 v24, v24, v25
	s_cbranch_scc1 .LBB0_1734
	s_lshl_b32 s20, s42, 4
	v_or_b32_e32 v22, s20, v119
	v_ashrrev_i32_e32 v23, 31, v22
	v_lshlrev_b64 v[26:27], 11, v[22:23]
	ds_swizzle_b32 v23, v24 offset:swizzle(SWAP,16)
	s_min_i32 s21, s20, 0x8000
	s_ashr_i32 s21, s21, 14
	s_mulk_i32 s21, 0x3000
	v_add_u32_e32 v133, s21, v127
	s_waitcnt lgkmcnt(0)
	v_add_f32_e32 v23, v24, v23
	v_mov_b32_e32 v24, v23
	s_nop 1
	v_permlane32_swap_b32_e32 v23, v24
	v_add_f32_e32 v23, v23, v24
	v_fmamk_f32 v23, v23, 0x3a800000, v224
	v_cmp_gt_f32_e32 vcc, s64, v23
	v_mul_f32_e32 v24, 0x4b800000, v23
	v_lshl_add_u64 v[114:115], v[92:93], 0, v[26:27]
	v_cndmask_b32_e32 v23, v23, v24, vcc
	v_rsq_f32_e32 v23, v23
	v_add_u32_e32 v109, 0x1000, v133
	v_mul_f32_e32 v24, 0x45800000, v23
	v_cndmask_b32_e32 v134, v23, v24, vcc
	s_or_b64 exec, exec, s[0:1]
	s_and_saveexec_b64 s[0:1], s[12:13]
	s_cbranch_execz .LBB0_1635
